# speedup vs baseline: 1.0643x; 1.0004x over previous
.LBB0_11:
	v_bfe_u32 v3, v0, 5, 1
	v_lshlrev_b32_e32 v4, 8, v0
	v_and_b32_e32 v4, 0x1f00, v4
	v_and_b32_e32 v5, 7, v0
	v_bitop3_b32 v6, v3, v0, 7 bitop3:0x78
	v_lshl_or_b32 v64, v6, 4, v4
	v_bitop3_b32 v6, v3, v5, 2 bitop3:0x36
	v_lshl_or_b32 v65, v6, 4, v4
	v_bitop3_b32 v6, v3, v5, 4 bitop3:0x36
	v_bitop3_b32 v5, v3, v5, 6 bitop3:0x36
	v_lshl_or_b32 v66, v6, 4, v4
	v_lshl_or_b32 v67, v5, 4, v4
	v_and_b32_e32 v4, 3, v0
	v_lshlrev_b32_e32 v6, 4, v0
	v_lshlrev_b32_e32 v5, 3, v4
	v_and_b32_e32 v6, 0xc0, v6
	v_lshlrev_b32_e32 v8, 1, v0
	v_lshlrev_b32_e32 v9, 8, v3
	v_bfe_u32 v7, v0, 4, 2
	v_and_b32_e32 v8, 32, v8
	v_or3_b32 v5, v5, v9, v6
	s_mov_b32 s0, 0x8000
	v_or3_b32 v184, v5, v8, s0
	v_lshlrev_b32_e32 v5, 8, v7
	v_xor_b32_e32 v6, v7, v1
	s_cmp_lg_u32 0, -1
	v_lshl_or_b32 v222, v6, 4, v5
	v_bitop3_b32 v1, v7, v1, 4 bitop3:0x36
	s_mov_b32 m0, s29
	s_nop 0
	buffer_load_dwordx4 v222, s[12:15], s61 offen lds
	s_cselect_b32 s17, 0, 0
	v_lshl_or_b32 v223, v1, 4, v5
	s_add_i32 s20, s29, 0x400
	s_add_i32 s0, s61, 0x400
	s_mov_b32 m0, s20
	s_nop 0
	buffer_load_dwordx4 v223, s[12:15], s0 offen lds
	v_lshlrev_b32_e32 v0, 6, v0
	s_add_i32 s21, s29, 0x800
	s_add_i32 s0, s61, 0x800
	s_mov_b32 m0, s21
	s_nop 0
	buffer_load_dwordx4 v222, s[12:15], s0 offen lds
	v_and_b32_e32 v0, 0x700, v0
	v_lshlrev_b32_e32 v1, 6, v3
	v_lshlrev_b32_e32 v3, 4, v4
	s_add_i32 s22, s29, 0xc00
	s_add_i32 s1, s61, 0xc00
	s_mov_b32 m0, s22
	s_nop 0
	buffer_load_dwordx4 v223, s[12:15], s1 offen lds
	v_or3_b32 v196, v0, v1, v3
	s_add_i32 s2, s29, 0x8000
	s_mov_b32 m0, s2
	s_nop 0
	buffer_load_dwordx4 v196, s[4:7], s61 offen lds
	s_add_i32 s1, s2, 0x400
	s_add_i32 s3, s61, 0x80
	s_mov_b32 m0, s1
	s_nop 0
	buffer_load_dwordx4 v196, s[4:7], s3 offen lds
	s_add_i32 s1, s2, 0x800
	s_mov_b32 m0, s1
	s_nop 0
	buffer_load_dwordx4 v196, s[4:7], s0 offen lds
	s_add_i32 s0, s2, 0xc00
	s_add_i32 s1, s61, 0x880
	s_mov_b32 m0, s0
	s_nop 0
	buffer_load_dwordx4 v196, s[4:7], s1 offen lds
	s_add_i32 s3, s29, 0x4000
	s_add_i32 s19, s61, 0x4000
	s_mov_b32 m0, s3
	s_nop 0
	buffer_load_dwordx4 v222, s[12:15], s19 offen lds
	v_or_b32_e32 v2, 0x10000, v40
	v_add_u32_e32 v218, s17, v64
	v_add_u32_e32 v219, s17, v65
	v_add_u32_e32 v220, s17, v66
	v_add_u32_e32 v221, s17, v67
	s_add_i32 s10, s29, 0x4400
	s_add_i32 s0, s61, 0x4400
	s_mov_b32 m0, s10
	s_nop 0
	buffer_load_dwordx4 v223, s[12:15], s0 offen lds
	s_add_i32 s11, s29, 0x4800
	s_add_i32 s18, s61, 0x4800
	s_mov_b32 m0, s11
	s_nop 0
	buffer_load_dwordx4 v222, s[12:15], s18 offen lds
	v_add_u32_e32 v32, v2, v218
	v_add_u32_e32 v33, v2, v219
	v_add_u32_e32 v34, v2, v220
	v_add_u32_e32 v35, v2, v221
	s_add_i32 s16, s29, 0x4c00
	s_add_i32 s0, s61, 0x4c00
	s_mov_b32 m0, s16
	s_nop 0
	buffer_load_dwordx4 v223, s[12:15], s0 offen lds
	v_add_u32_e32 v212, s17, v184
	ds_read_b128 v[0:3], v32 offset:0
	ds_read_b128 v[4:7], v33 offset:0
	ds_read_b128 v[8:11], v34 offset:0
	ds_read_b128 v[12:15], v35 offset:0
	ds_read_b128 v[16:19], v32 offset:128
	ds_read_b128 v[20:23], v33 offset:128
	ds_read_b128 v[24:27], v34 offset:128
	ds_read_b128 v[28:31], v35 offset:128
	s_waitcnt lgkmcnt(0)
	v_accvgpr_write_b32 a[128], v0
	v_accvgpr_write_b32 a[129], v1
	v_accvgpr_write_b32 a[130], v2
	v_accvgpr_write_b32 a[131], v3
	v_accvgpr_write_b32 a[132], v4
	v_accvgpr_write_b32 a[133], v5
	v_accvgpr_write_b32 a[134], v6
	v_accvgpr_write_b32 a[135], v7
	v_accvgpr_write_b32 a[136], v8
	v_accvgpr_write_b32 a[137], v9
	v_accvgpr_write_b32 a[138], v10
	v_accvgpr_write_b32 a[139], v11
	v_accvgpr_write_b32 a[140], v12
	v_accvgpr_write_b32 a[141], v13
	v_accvgpr_write_b32 a[142], v14
	v_accvgpr_write_b32 a[143], v15
	v_accvgpr_write_b32 a[144], v16
	v_accvgpr_write_b32 a[145], v17
	v_accvgpr_write_b32 a[146], v18
	v_accvgpr_write_b32 a[147], v19
	v_accvgpr_write_b32 a[148], v20
	v_accvgpr_write_b32 a[149], v21
	v_accvgpr_write_b32 a[150], v22
	v_accvgpr_write_b32 a[151], v23
	v_accvgpr_write_b32 a[152], v24
	v_accvgpr_write_b32 a[153], v25
	v_accvgpr_write_b32 a[154], v26
	v_accvgpr_write_b32 a[155], v27
	v_accvgpr_write_b32 a[156], v28
	v_accvgpr_write_b32 a[157], v29
	v_accvgpr_write_b32 a[158], v30
	v_accvgpr_write_b32 a[159], v31
	ds_read_b128 v[0:3], v32 offset:8192
	ds_read_b128 v[4:7], v33 offset:8192
	ds_read_b128 v[8:11], v34 offset:8192
	ds_read_b128 v[12:15], v35 offset:8192
	ds_read_b128 v[16:19], v32 offset:8320
	ds_read_b128 v[20:23], v33 offset:8320
	ds_read_b128 v[24:27], v34 offset:8320
	ds_read_b128 v[28:31], v35 offset:8320
	s_waitcnt lgkmcnt(0)
	v_accvgpr_write_b32 a[160], v0
	v_accvgpr_write_b32 a[161], v1
	v_accvgpr_write_b32 a[162], v2
	v_accvgpr_write_b32 a[163], v3
	v_accvgpr_write_b32 a[164], v4
	v_accvgpr_write_b32 a[165], v5
	v_accvgpr_write_b32 a[166], v6
	v_accvgpr_write_b32 a[167], v7
	v_accvgpr_write_b32 a[168], v8
	v_accvgpr_write_b32 a[169], v9
	v_accvgpr_write_b32 a[170], v10
	v_accvgpr_write_b32 a[171], v11
	v_accvgpr_write_b32 a[172], v12
	v_accvgpr_write_b32 a[173], v13
	v_accvgpr_write_b32 a[174], v14
	v_accvgpr_write_b32 a[175], v15
	v_accvgpr_write_b32 a[176], v16
	v_accvgpr_write_b32 a[177], v17
	v_accvgpr_write_b32 a[178], v18
	v_accvgpr_write_b32 a[179], v19
	v_accvgpr_write_b32 a[180], v20
	v_accvgpr_write_b32 a[181], v21
	v_accvgpr_write_b32 a[182], v22
	v_accvgpr_write_b32 a[183], v23
	v_accvgpr_write_b32 a[184], v24
	v_accvgpr_write_b32 a[185], v25
	v_accvgpr_write_b32 a[186], v26
	v_accvgpr_write_b32 a[187], v27
	v_accvgpr_write_b32 a[188], v28
	v_accvgpr_write_b32 a[189], v29
	v_accvgpr_write_b32 a[190], v30
	v_accvgpr_write_b32 a[191], v31
	s_waitcnt vmcnt(0) lgkmcnt(0)
	s_barrier
	s_nop 0
	ds_read_b128 a[192:195], v218 offset:0
	s_nop 0
	ds_read_b128 a[196:199], v219 offset:0
	ds_read_b128 a[200:203], v220 offset:0
	ds_read_b128 a[204:207], v221 offset:0
	ds_read_b128 a[208:211], v218 offset:128
	ds_read_b128 a[212:215], v219 offset:128
	ds_read_b128 a[216:219], v220 offset:128
	ds_read_b128 a[220:223], v221 offset:128
	ds_read_b128 a[224:227], v218 offset:8192
	ds_read_b128 a[228:231], v219 offset:8192
	ds_read_b128 a[232:235], v220 offset:8192
	ds_read_b128 a[236:239], v221 offset:8192
	ds_read_b128 a[240:243], v218 offset:8320
	ds_read_b128 a[244:247], v219 offset:8320
	ds_read_b128 a[248:251], v220 offset:8320
	ds_read_b128 a[252:255], v221 offset:8320
	s_waitcnt lgkmcnt(0)
	v_mfma_f32_32x32x16_bf16 v[48:63], a[192:195], a[128:131], 0
	v_mfma_f32_32x32x16_bf16 v[32:47], a[192:195], a[160:163], 0
	v_mfma_f32_32x32x16_bf16 v[0:15], a[224:227], a[128:131], 0
	v_mfma_f32_32x32x16_bf16 v[16:31], a[224:227], a[160:163], 0
	v_mfma_f32_32x32x16_bf16 v[48:63], a[196:199], a[132:135], v[48:63]
	v_mfma_f32_32x32x16_bf16 v[32:47], a[196:199], a[164:167], v[32:47]
	v_mfma_f32_32x32x16_bf16 v[0:15], a[228:231], a[132:135], v[0:15]
	v_mfma_f32_32x32x16_bf16 v[16:31], a[228:231], a[164:167], v[16:31]
	v_mfma_f32_32x32x16_bf16 v[48:63], a[200:203], a[136:139], v[48:63]
	v_mfma_f32_32x32x16_bf16 v[32:47], a[200:203], a[168:171], v[32:47]
	v_mfma_f32_32x32x16_bf16 v[0:15], a[232:235], a[136:139], v[0:15]
	v_mfma_f32_32x32x16_bf16 v[16:31], a[232:235], a[168:171], v[16:31]
	v_mfma_f32_32x32x16_bf16 v[48:63], a[204:207], a[140:143], v[48:63]
	v_mfma_f32_32x32x16_bf16 v[32:47], a[204:207], a[172:175], v[32:47]
	v_mfma_f32_32x32x16_bf16 v[0:15], a[236:239], a[140:143], v[0:15]
	v_mfma_f32_32x32x16_bf16 v[16:31], a[236:239], a[172:175], v[16:31]
	v_mfma_f32_32x32x16_bf16 v[48:63], a[208:211], a[144:147], v[48:63]
	s_mov_b32 s27, s29
	v_mfma_f32_32x32x16_bf16 v[32:47], a[208:211], a[176:179], v[32:47]
	s_add_i32 s0, s62, 0x0
	s_mov_b32 s30, s0
	v_mfma_f32_32x32x16_bf16 v[0:15], a[240:243], a[144:147], v[0:15]
	s_mov_b32 s31, s20
	v_mfma_f32_32x32x16_bf16 v[16:31], a[240:243], a[176:179], v[16:31]
	s_add_i32 s33, s62, 0x400
	v_mfma_f32_32x32x16_bf16 v[48:63], a[212:215], a[148:151], v[48:63]
	s_mov_b32 s34, s21
	v_mfma_f32_32x32x16_bf16 v[32:47], a[212:215], a[180:183], v[32:47]
	s_add_i32 s1, s62, 0x800
	s_mov_b32 s35, s1
	v_mfma_f32_32x32x16_bf16 v[0:15], a[244:247], a[148:151], v[0:15]
	s_mov_b32 s36, s22
	v_mfma_f32_32x32x16_bf16 v[16:31], a[244:247], a[180:183], v[16:31]
	s_add_i32 s37, s62, 0xc00
	v_mfma_f32_32x32x16_bf16 v[48:63], a[216:219], a[152:155], v[48:63]
	s_add_i32 s23, s29, 0xc000
	s_mov_b32 s38, s23
	v_mfma_f32_32x32x16_bf16 v[32:47], a[216:219], a[184:187], v[32:47]
	v_mfma_f32_32x32x16_bf16 v[0:15], a[248:251], a[152:155], v[0:15]
	s_add_i32 s24, s29, 0xc400
	s_mov_b32 s39, s24
	v_mfma_f32_32x32x16_bf16 v[16:31], a[248:251], a[184:187], v[16:31]
	s_add_i32 s40, s61, 0x4080
	v_mfma_f32_32x32x16_bf16 v[48:63], a[220:223], a[156:159], v[48:63]
	s_add_i32 s25, s29, 0xc800
	s_mov_b32 s41, s25
	v_mfma_f32_32x32x16_bf16 v[32:47], a[220:223], a[188:191], v[32:47]
	v_mfma_f32_32x32x16_bf16 v[0:15], a[252:255], a[156:159], v[0:15]
	s_add_i32 s26, s29, 0xcc00
	s_mov_b32 s42, s26
	v_mfma_f32_32x32x16_bf16 v[16:31], a[252:255], a[188:191], v[16:31]
	s_add_i32 s43, s61, 0x4880
	s_nop 0
	s_nop 4
	s_waitcnt vmcnt(0) lgkmcnt(0)
	s_barrier
	s_nop 0
	s_mov_b32 m0, s27
	s_nop 0
	buffer_load_dwordx4 v222, s[12:15], s30 offen lds
	s_mov_b32 m0, s31
	s_nop 0
	buffer_load_dwordx4 v223, s[12:15], s33 offen lds
	s_addk_i32 s17, 0x4000
	v_add_u32_e32 v217, s17, v64
	ds_read_b128 a[192:195], v217 offset:0
	s_mov_b32 m0, s34
	s_nop 0
	buffer_load_dwordx4 v222, s[12:15], s35 offen lds
	v_add_u32_e32 v199, s17, v65
	ds_read_b128 a[196:199], v199 offset:0
	s_mov_b32 m0, s36
	s_nop 0
	buffer_load_dwordx4 v223, s[12:15], s37 offen lds
	v_add_u32_e32 v198, s17, v66
	ds_read_b128 a[200:203], v198 offset:0
	s_mov_b32 m0, s38
	s_nop 0
	buffer_load_dwordx4 v196, s[4:7], s19 offen lds
	v_add_u32_e32 v197, s17, v67
	ds_read_b128 a[204:207], v197 offset:0
	s_mov_b32 m0, s39
	s_nop 0
	buffer_load_dwordx4 v196, s[4:7], s40 offen lds
	ds_read_b128 a[208:211], v217 offset:128
	s_mov_b32 m0, s41
	s_nop 0
	buffer_load_dwordx4 v196, s[4:7], s18 offen lds
	ds_read_b128 a[212:215], v199 offset:128
	s_mov_b32 m0, s42
	s_nop 0
	buffer_load_dwordx4 v196, s[4:7], s43 offen lds
	ds_read_b128 a[216:219], v198 offset:128
	ds_read_b128 a[220:223], v197 offset:128
	v_cvt_pk_bf16_f32 v248, v248, v249
	v_cvt_pk_bf16_f32 v249, v250, v251
	v_cvt_pk_bf16_f32 v250, v252, v253
	v_cvt_pk_bf16_f32 v251, v254, v255
	v_lshrrev_b32_e32 v252, 1, v208
	buffer_store_dwordx4 v[248:251], v252, s[12:15], s56 offen sc1
	s_nop 1
	global_load_dwordx4 v[248:251], v208, s[74:75] nt
	global_load_dwordx4 v[252:255], v208, s[74:75] offset:16 nt
	s_add_u32 s74, s74, 0x2000
	s_addc_u32 s75, s75, 0
	v_max3_f32 v64, v48, v49, v0
	v_max3_f32 v65, v50, v51, v1
	v_max3_f32 v64, v64, v2, v3
	ds_read_b128 a[224:227], v217 offset:8192
	v_max3_f32 v64, v64, v52, v53
	v_max3_f32 v65, v65, v54, v55
	v_max3_f32 v64, v64, v4, v5
	v_max3_f32 v65, v65, v6, v7
	ds_read_b128 a[228:231], v199 offset:8192
	v_max3_f32 v64, v64, v56, v57
	v_max3_f32 v65, v65, v58, v59
	v_max3_f32 v64, v64, v8, v9
	v_max3_f32 v65, v65, v10, v11
	ds_read_b128 a[232:235], v198 offset:8192
	v_max3_f32 v64, v64, v60, v61
	v_max3_f32 v65, v65, v62, v63
	v_max3_f32 v64, v64, v12, v13
	v_max3_f32 v65, v65, v14, v15
	ds_read_b128 a[236:239], v197 offset:8192
	v_max3_f32 v66, v32, v33, v16
	v_max3_f32 v67, v34, v35, v17
	v_max3_f32 v66, v66, v18, v19
	ds_read_b128 a[240:243], v217 offset:8320
	v_max3_f32 v66, v66, v36, v37
	v_max3_f32 v67, v67, v38, v39
	v_max3_f32 v66, v66, v20, v21
	v_max3_f32 v67, v67, v22, v23
	ds_read_b128 a[244:247], v199 offset:8320
	v_max3_f32 v66, v66, v40, v41
	v_max3_f32 v67, v67, v42, v43
	v_max3_f32 v66, v66, v24, v25
	v_max3_f32 v67, v67, v26, v27
	ds_read_b128 a[248:251], v198 offset:8320
	v_max3_f32 v66, v66, v44, v45
	v_max3_f32 v67, v67, v46, v47
	v_max3_f32 v66, v66, v28, v29
	v_max3_f32 v67, v67, v30, v31
	ds_read_b128 a[252:255], v197 offset:8320
	v_max_f32_e32 v64, v64, v65
	v_mov_b32_e32 v65, v64
	s_nop 1
	v_permlane32_swap_b32_e32 v64, v65
	v_max_f32_e32 v214, v64, v65
	v_max_f32_e32 v64, v66, v67
	v_mov_b32_e32 v65, v64
	s_nop 1
	v_permlane32_swap_b32_e32 v64, v65
	v_max_f32_e32 v213, v64, v65
	v_sub_f32_e32 v64, v0, v214
	v_mbcnt_lo_u32_b32 v0, -1, 0
	v_mbcnt_hi_u32_b32 v0, -1, v0
	v_sub_f32_e32 v65, v1, v214
	v_xor_b32_e32 v1, 0x80000000, v214
	v_cmp_gt_u32_e32 vcc, 32, v0
	v_sub_f32_e32 v128, v2, v214
	v_sub_f32_e32 v129, v3, v214
	v_sub_f32_e32 v130, v4, v214
	v_sub_f32_e32 v131, v5, v214
	v_sub_f32_e32 v132, v6, v214
	v_sub_f32_e32 v133, v7, v214
	v_sub_f32_e32 v134, v8, v214
	v_sub_f32_e32 v135, v9, v214
	v_sub_f32_e32 v136, v10, v214
	v_sub_f32_e32 v137, v11, v214
	v_sub_f32_e32 v138, v12, v214
	v_sub_f32_e32 v139, v13, v214
	v_sub_f32_e32 v140, v14, v214
	v_sub_f32_e32 v141, v15, v214
	v_sub_f32_e32 v142, v16, v213
	v_mov_b32_e32 v211, 1.0
	v_sub_f32_e32 v143, v17, v213
	v_xor_b32_e32 v17, 0x80000000, v213
	v_cndmask_b32_e64 v0, 0, 1.0, vcc
	s_nop 1
	v_mfma_f32_32x32x2_f32 v[0:15], v0, v1, 0
	v_mbcnt_lo_u32_b32 v16, -1, 0
	v_mbcnt_hi_u32_b32 v16, -1, v16
	v_sub_f32_e32 v48, v48, v214
	v_sub_f32_e32 v49, v49, v214
	v_sub_f32_e32 v50, v50, v214
	v_sub_f32_e32 v51, v51, v214
	v_sub_f32_e32 v52, v52, v214
	v_sub_f32_e32 v53, v53, v214
	v_sub_f32_e32 v54, v54, v214
	v_sub_f32_e32 v55, v55, v214
	v_sub_f32_e32 v56, v56, v214
	v_sub_f32_e32 v57, v57, v214
	v_sub_f32_e32 v58, v58, v214
	v_sub_f32_e32 v59, v59, v214
	v_sub_f32_e32 v60, v60, v214
	v_sub_f32_e32 v61, v61, v214
	v_sub_f32_e32 v62, v62, v214
	v_sub_f32_e32 v63, v63, v214
	v_sub_f32_e32 v32, v32, v213
	v_sub_f32_e32 v33, v33, v213
	v_sub_f32_e32 v34, v34, v213
	v_cmp_gt_u32_e32 vcc, 32, v16
	v_sub_f32_e32 v35, v35, v213
	v_sub_f32_e32 v36, v36, v213
	v_sub_f32_e32 v37, v37, v213
	v_sub_f32_e32 v38, v38, v213
	v_sub_f32_e32 v39, v39, v213
	v_sub_f32_e32 v40, v40, v213
	v_sub_f32_e32 v41, v41, v213
	v_sub_f32_e32 v42, v42, v213
	v_sub_f32_e32 v43, v43, v213
	v_sub_f32_e32 v44, v44, v213
	v_sub_f32_e32 v45, v45, v213
	v_sub_f32_e32 v46, v46, v213
	v_sub_f32_e32 v47, v47, v213
	v_sub_f32_e32 v144, v18, v213
	v_sub_f32_e32 v145, v19, v213
	v_sub_f32_e32 v146, v20, v213
	v_sub_f32_e32 v147, v21, v213
	v_sub_f32_e32 v183, v22, v213
	v_sub_f32_e32 v194, v23, v213
	v_cndmask_b32_e64 v16, 0, 1.0, vcc
	v_sub_f32_e32 v195, v24, v213
	v_sub_f32_e32 v215, v25, v213
	v_sub_f32_e32 v216, v26, v213
	v_sub_f32_e32 v224, v27, v213
	v_sub_f32_e32 v225, v28, v213
	v_sub_f32_e32 v226, v29, v213
	v_sub_f32_e32 v229, v30, v213
	v_sub_f32_e32 v230, v31, v213
	v_mfma_f32_32x32x2_f32 v[16:31], v16, v17, 0
	v_exp_f32_e32 v112, v48
	v_exp_f32_e32 v113, v49
	v_exp_f32_e32 v114, v50
	v_exp_f32_e32 v115, v51
	v_mov_b32_e32 v193, 0
	v_add_f32_e32 v48, v193, v112
	v_add_f32_e32 v49, v193, v113
	v_exp_f32_e32 v116, v52
	v_exp_f32_e32 v117, v53
	v_exp_f32_e32 v118, v54
	v_add_f32_e32 v48, v48, v114
	v_add_f32_e32 v49, v49, v115
	v_exp_f32_e32 v119, v55
	v_exp_f32_e32 v120, v56
	v_add_f32_e32 v48, v48, v116
	v_add_f32_e32 v49, v49, v117
	v_add_f32_e32 v48, v48, v118
	v_exp_f32_e32 v121, v57
	v_exp_f32_e32 v122, v58
	v_exp_f32_e32 v123, v59
	v_add_f32_e32 v49, v49, v119
	v_add_f32_e32 v48, v48, v120
	v_exp_f32_e32 v124, v60
	v_exp_f32_e32 v125, v61
	v_add_f32_e32 v49, v49, v121
	v_add_f32_e32 v48, v48, v122
	v_add_f32_e32 v49, v49, v123
	v_exp_f32_e32 v126, v62
	v_exp_f32_e32 v127, v63
	v_exp_f32_e32 v96, v32
	v_add_f32_e32 v32, v48, v124
	v_add_f32_e32 v48, v49, v125
	v_exp_f32_e32 v97, v33
	v_exp_f32_e32 v98, v34
	v_add_f32_e32 v231, v32, v126
	v_add_f32_e32 v232, v48, v127
	v_add_f32_e32 v32, v193, v96
	v_exp_f32_e32 v99, v35
	v_exp_f32_e32 v100, v36
	v_exp_f32_e32 v101, v37
	v_add_f32_e32 v33, v193, v97
	v_add_f32_e32 v32, v32, v98
	v_exp_f32_e32 v102, v38
	v_exp_f32_e32 v103, v39
	v_add_f32_e32 v33, v33, v99
	v_add_f32_e32 v32, v32, v100
	v_add_f32_e32 v33, v33, v101
	v_exp_f32_e32 v104, v40
	v_exp_f32_e32 v105, v41
	v_exp_f32_e32 v106, v42
	v_add_f32_e32 v32, v32, v102
	v_add_f32_e32 v33, v33, v103
	v_exp_f32_e32 v107, v43
	v_exp_f32_e32 v108, v44
	v_add_f32_e32 v32, v32, v104
	v_add_f32_e32 v33, v33, v105
	v_add_f32_e32 v32, v32, v106
	v_exp_f32_e32 v109, v45
	v_exp_f32_e32 v110, v46
	v_exp_f32_e32 v111, v47
	v_add_f32_e32 v33, v33, v107
	v_add_f32_e32 v32, v32, v108
	s_waitcnt lgkmcnt(0)
	v_add_f32_e32 v33, v33, v109
	v_add_f32_e32 v233, v32, v110
	v_add_f32_e32 v234, v33, v111
	v_mfma_f32_32x32x16_bf16 v[80:95], a[192:195], a[128:131], v[0:15]
	ds_read_b64_tr_b16 v[160:161], v212 offset:0
	v_exp_f32_e32 v235, v64
	v_exp_f32_e32 v236, v65
	v_cvt_pk_bf16_f32 v152, v112, v113
	v_mfma_f32_32x32x16_bf16 v[64:79], a[192:195], a[160:163], v[16:31]
	ds_read_b64_tr_b16 v[162:163], v212 offset:0x800
	v_exp_f32_e32 v237, v128
	v_exp_f32_e32 v238, v129
	v_cvt_pk_bf16_f32 v153, v114, v115
	v_exp_f32_e32 v115, v130
	v_mfma_f32_32x32x16_bf16 v[48:63], a[224:227], a[128:131], v[0:15]
	ds_read_b64_tr_b16 v[172:173], v212 offset:0x200
	v_exp_f32_e32 v239, v131
	v_cvt_pk_bf16_f32 v154, v116, v117
	v_mfma_f32_32x32x16_bf16 v[32:47], a[224:227], a[160:163], v[16:31]
	ds_read_b64_tr_b16 v[174:175], v212 offset:0xa00
	ds_read_b64_tr_b16 v[168:169], v212 offset:0x400
	v_exp_f32_e32 v240, v132
	v_exp_f32_e32 v241, v133
	v_cvt_pk_bf16_f32 v155, v118, v119
	v_exp_f32_e32 v185, v134
	v_exp_f32_e32 v186, v135
	v_mfma_f32_32x32x16_bf16 v[80:95], a[196:199], a[132:135], v[80:95]
	ds_read_b64_tr_b16 v[170:171], v212 offset:0xc00
	v_cvt_pk_bf16_f32 v128, v120, v121
	v_exp_f32_e32 v187, v136
	v_exp_f32_e32 v188, v137
	v_mfma_f32_32x32x16_bf16 v[64:79], a[196:199], a[164:167], v[64:79]
	ds_read_b64_tr_b16 v[176:177], v212 offset:0x600
	v_cvt_pk_bf16_f32 v129, v122, v123
	v_exp_f32_e32 v189, v138
	v_exp_f32_e32 v190, v139
	v_mfma_f32_32x32x16_bf16 v[48:63], a[228:231], a[132:135], v[48:63]
	ds_read_b64_tr_b16 v[178:179], v212 offset:0xe00
	v_cvt_pk_bf16_f32 v130, v124, v125
	v_mfma_f32_32x32x16_bf16 v[32:47], a[228:231], a[164:167], v[32:47]
	ds_read_b64_tr_b16 v[164:165], v212 offset:0x1000
	v_exp_f32_e32 v191, v140
	v_exp_f32_e32 v192, v141
	ds_read_b64_tr_b16 v[166:167], v212 offset:0x1800
	v_cvt_pk_bf16_f32 v131, v126, v127
	v_exp_f32_e32 v141, v142
	v_exp_f32_e32 v142, v143
	v_mfma_f32_32x32x16_bf16 v[80:95], a[200:203], a[136:139], v[80:95]
	ds_read_b64_tr_b16 v[156:157], v212 offset:0x1200
	v_cvt_pk_bf16_f32 v180, v96, v97
	v_exp_f32_e32 v143, v144
	v_mfma_f32_32x32x16_bf16 v[64:79], a[200:203], a[168:171], v[64:79]
	ds_read_b64_tr_b16 v[158:159], v212 offset:0x1a00
	v_exp_f32_e32 v242, v145
	v_cvt_pk_bf16_f32 v181, v98, v99
	v_mfma_f32_32x32x16_bf16 v[48:63], a[232:235], a[136:139], v[48:63]
	ds_read_b64_tr_b16 v[148:149], v212 offset:0x1400
	v_exp_f32_e32 v243, v146
	v_exp_f32_e32 v244, v147
	v_cvt_pk_bf16_f32 v182, v100, v101
	v_mfma_f32_32x32x16_bf16 v[32:47], a[232:235], a[168:171], v[32:47]
	ds_read_b64_tr_b16 v[150:151], v212 offset:0x1c00
	ds_read_b64_tr_b16 v[136:137], v212 offset:0x1600
	v_exp_f32_e32 v245, v183
	v_exp_f32_e32 v246, v194
	v_cvt_pk_bf16_f32 v183, v102, v103
	v_exp_f32_e32 v194, v195
	v_exp_f32_e32 v195, v215
	v_mfma_f32_32x32x16_bf16 v[80:95], a[204:207], a[140:143], v[80:95]
	ds_read_b64_tr_b16 v[138:139], v212 offset:0x1e00
	v_cvt_pk_bf16_f32 v144, v104, v105
	v_exp_f32_e32 v215, v216
	v_exp_f32_e32 v224, v224
	v_mfma_f32_32x32x16_bf16 v[64:79], a[204:207], a[172:175], v[64:79]
	ds_read_b64_tr_b16 v[132:133], v212 offset:0x2000
	v_cvt_pk_bf16_f32 v145, v106, v107
	v_exp_f32_e32 v227, v225
	v_exp_f32_e32 v228, v226
	v_mfma_f32_32x32x16_bf16 v[48:63], a[236:239], a[140:143], v[48:63]
	ds_read_b64_tr_b16 v[134:135], v212 offset:0x2800
	v_cvt_pk_bf16_f32 v146, v108, v109
	v_mfma_f32_32x32x16_bf16 v[32:47], a[236:239], a[172:175], v[32:47]
	ds_read_b64_tr_b16 v[124:125], v212 offset:0x2200
	v_exp_f32_e32 v229, v229
	v_exp_f32_e32 v230, v230
	ds_read_b64_tr_b16 v[126:127], v212 offset:0x2a00
	v_cvt_pk_bf16_f32 v147, v110, v111
	s_mov_b32 s27, s3
	v_mfma_f32_32x32x16_bf16 v[80:95], a[208:211], a[144:147], v[80:95]
	ds_read_b64_tr_b16 v[120:121], v212 offset:0x2400
	v_cvt_pk_bf16_f32 v112, v235, v236
	v_add_f32_e32 v96, v231, v235
	v_add_f32_e32 v97, v232, v236
	s_add_i32 s30, s62, 0x4000
	v_mfma_f32_32x32x16_bf16 v[64:79], a[208:211], a[176:179], v[64:79]
	ds_read_b64_tr_b16 v[122:123], v212 offset:0x2c00
	v_cvt_pk_bf16_f32 v113, v237, v238
	v_add_f32_e32 v96, v96, v237
	v_add_f32_e32 v97, v97, v238
	s_mov_b32 s31, s10
	v_mfma_f32_32x32x16_bf16 v[48:63], a[240:243], a[144:147], v[48:63]
	ds_read_b64_tr_b16 v[116:117], v212 offset:0x2600
	v_cvt_pk_bf16_f32 v114, v115, v239
	v_add_f32_e32 v96, v96, v115
	v_add_f32_e32 v97, v97, v239
	s_add_i32 s33, s62, 0x4400
	v_mfma_f32_32x32x16_bf16 v[32:47], a[240:243], a[176:179], v[32:47]
	ds_read_b64_tr_b16 v[118:119], v212 offset:0x2e00
	ds_read_b64_tr_b16 v[104:105], v212 offset:0x3000
	v_cvt_pk_bf16_f32 v115, v240, v241
	v_add_f32_e32 v96, v96, v240
	v_add_f32_e32 v97, v97, v241
	s_mov_b32 s34, s11
	v_mfma_f32_32x32x16_bf16 v[80:95], a[212:215], a[148:151], v[80:95]
	ds_read_b64_tr_b16 v[106:107], v212 offset:0x3800
	v_add_f32_e32 v96, v96, v185
	v_add_f32_e32 v97, v97, v186
	s_add_i32 s35, s62, 0x4800
	v_mfma_f32_32x32x16_bf16 v[64:79], a[212:215], a[180:183], v[64:79]
	ds_read_b64_tr_b16 v[108:109], v212 offset:0x3200
	v_add_f32_e32 v96, v96, v187
	v_add_f32_e32 v97, v97, v188
	s_mov_b32 s36, s16
	v_mfma_f32_32x32x16_bf16 v[48:63], a[244:247], a[148:151], v[48:63]
	ds_read_b64_tr_b16 v[110:111], v212 offset:0x3a00
	v_add_f32_e32 v96, v96, v189
	v_add_f32_e32 v97, v97, v190
	s_add_i32 s37, s62, 0x4c00
	v_mfma_f32_32x32x16_bf16 v[32:47], a[244:247], a[180:183], v[32:47]
	ds_read_b64_tr_b16 v[100:101], v212 offset:0x3400
	ds_read_b64_tr_b16 v[102:103], v212 offset:0x3c00
	v_add_f32_e32 v216, v96, v191
	v_add_f32_e32 v225, v97, v192
	s_mov_b32 s38, s2
	v_mfma_f32_32x32x16_bf16 v[80:95], a[216:219], a[152:155], v[80:95]
	ds_read_b64_tr_b16 v[96:97], v212 offset:0x3600
	v_cvt_pk_bf16_f32 v140, v141, v142
	v_add_f32_e32 v226, v233, v141
	v_add_f32_e32 v142, v234, v142
	v_mfma_f32_32x32x16_bf16 v[64:79], a[216:219], a[184:187], v[64:79]
	ds_read_b64_tr_b16 v[98:99], v212 offset:0x3e00
	v_cvt_pk_bf16_f32 v141, v143, v242
	v_add_f32_e32 v143, v226, v143
	v_add_f32_e32 v226, v142, v242
	v_mfma_f32_32x32x16_bf16 v[48:63], a[248:251], a[152:155], v[48:63]
	s_add_i32 s17, s29, 0x8400
	s_mov_b32 s39, s17
	v_cvt_pk_bf16_f32 v142, v243, v244
	v_add_f32_e32 v231, v143, v243
	v_add_f32_e32 v226, v226, v244
	v_mfma_f32_32x32x16_bf16 v[32:47], a[248:251], a[184:187], v[32:47]
	s_add_i32 s40, s62, 0x80
	v_cvt_pk_bf16_f32 v143, v245, v246
	v_add_f32_e32 v231, v231, v245
	v_add_f32_e32 v226, v226, v246
	v_mfma_f32_32x32x16_bf16 v[80:95], a[220:223], a[156:159], v[80:95]
	s_add_i32 s18, s29, 0x8800
	s_mov_b32 s41, s18
	v_add_f32_e32 v231, v231, v194
	v_add_f32_e32 v226, v226, v195
	v_mfma_f32_32x32x16_bf16 v[64:79], a[220:223], a[188:191], v[64:79]
	v_add_f32_e32 v231, v231, v215
	v_add_f32_e32 v226, v226, v224
	v_mfma_f32_32x32x16_bf16 v[48:63], a[252:255], a[156:159], v[48:63]
	s_add_i32 s19, s29, 0x8c00
	s_mov_b32 s42, s19
	v_add_f32_e32 v231, v231, v227
	v_add_f32_e32 v226, v226, v228
	v_mfma_f32_32x32x16_bf16 v[32:47], a[252:255], a[188:191], v[32:47]
	s_add_i32 s43, s62, 0x880
	v_add_f32_e32 v231, v231, v229
	v_add_f32_e32 v226, v226, v230
	s_nop 0
	s_nop 4
	v_add_f32_e32 v216, v216, v225
	s_waitcnt vmcnt(0) lgkmcnt(0)
	s_barrier
	v_mfma_f32_32x32x16_bf16 a[0:15], v[160:163], v[152:155], 0
	v_mov_b32_e32 v225, v216
	s_mov_b32 m0, s27
	s_nop 0
	buffer_load_dwordx4 v222, s[12:15], s30 offen lds
	v_mfma_f32_32x32x16_bf16 a[16:31], v[160:163], v[180:183], 0
	v_permlane32_swap_b32_e32 v216, v225
	v_add_f32_e32 v216, v216, v225
	s_mov_b32 m0, s31
	s_nop 0
	buffer_load_dwordx4 v223, s[12:15], s33 offen lds
	ds_read_b128 a[192:195], v218 offset:0
	v_mfma_f32_32x32x16_bf16 a[32:47], v[172:175], v[152:155], 0
	v_add_f32_e32 v225, v193, v216
	v_add_f32_e32 v216, v231, v226
	v_mov_b32_e32 v226, v216
	s_mov_b32 m0, s34
	s_nop 0
	buffer_load_dwordx4 v222, s[12:15], s35 offen lds
	ds_read_b128 a[196:199], v219 offset:0
	v_mfma_f32_32x32x16_bf16 a[48:63], v[172:175], v[180:183], 0
	v_permlane32_swap_b32_e32 v216, v226
	v_add_f32_e32 v216, v216, v226
	s_mov_b32 m0, s36
	s_nop 0
	buffer_load_dwordx4 v223, s[12:15], s37 offen lds
	ds_read_b128 a[200:203], v220 offset:0
	v_mfma_f32_32x32x16_bf16 a[64:79], v[168:171], v[152:155], 0
	v_add_f32_e32 v226, v193, v216
	s_mov_b32 m0, s38
	s_nop 0
	buffer_load_dwordx4 v196, s[4:7], s0 offen lds
	ds_read_b128 a[204:207], v221 offset:0
	v_mfma_f32_32x32x16_bf16 a[80:95], v[168:171], v[180:183], 0
	s_mov_b32 m0, s39
	s_nop 0
	buffer_load_dwordx4 v196, s[4:7], s40 offen lds
	ds_read_b128 a[208:211], v218 offset:128
	v_mfma_f32_32x32x16_bf16 a[96:111], v[176:179], v[152:155], 0
	s_mov_b32 m0, s41
	s_nop 0
	buffer_load_dwordx4 v196, s[4:7], s1 offen lds
	ds_read_b128 a[212:215], v219 offset:128
	v_mfma_f32_32x32x16_bf16 a[112:127], v[176:179], v[180:183], 0
	s_mov_b32 m0, s42
	s_nop 0
	buffer_load_dwordx4 v196, s[4:7], s43 offen lds
	ds_read_b128 a[216:219], v220 offset:128
	v_mfma_f32_32x32x16_bf16 a[0:15], v[164:167], v[128:131], a[0:15]
	ds_read_b128 a[220:223], v221 offset:128
	v_pk_add_f32 v[200:201], v[248:249], v[200:201]
	v_pk_add_f32 v[202:203], v[250:251], v[202:203]
	v_pk_add_f32 v[204:205], v[252:253], v[204:205]
	v_pk_add_f32 v[206:207], v[254:255], v[206:207]
	v_cvt_pk_bf16_f32 v248, v248, v249
	v_cvt_pk_bf16_f32 v249, v250, v251
	v_cvt_pk_bf16_f32 v250, v252, v253
	v_cvt_pk_bf16_f32 v251, v254, v255
	v_lshrrev_b32_e32 v252, 1, v208
	buffer_store_dwordx4 v[248:251], v252, s[4:7], s56 offen sc1
	s_add_i32 s56, s56, 0x1000
	s_nop 1
	global_load_dwordx4 v[248:251], v208, s[54:55] nt
	global_load_dwordx4 v[252:255], v208, s[54:55] offset:16 nt
	s_add_u32 s54, s54, 0x2000
	s_addc_u32 s55, s55, 0
	v_max3_f32 v152, v80, v81, v48
	v_max3_f32 v153, v82, v83, v49
	v_max3_f32 v152, v152, v50, v51
	v_mfma_f32_32x32x16_bf16 a[16:31], v[164:167], v[144:147], a[16:31]
	ds_read_b128 a[224:227], v218 offset:8192
	v_max3_f32 v152, v152, v84, v85
	v_max3_f32 v153, v153, v86, v87
	v_max3_f32 v152, v152, v52, v53
	v_max3_f32 v153, v153, v54, v55
	v_mfma_f32_32x32x16_bf16 a[32:47], v[156:159], v[128:131], a[32:47]
	ds_read_b128 a[228:231], v219 offset:8192
	v_max3_f32 v152, v152, v88, v89
	v_max3_f32 v153, v153, v90, v91
	v_max3_f32 v152, v152, v56, v57
	v_max3_f32 v153, v153, v58, v59
	v_mfma_f32_32x32x16_bf16 a[48:63], v[156:159], v[144:147], a[48:63]
	ds_read_b128 a[232:235], v220 offset:8192
	v_max3_f32 v152, v152, v92, v93
	v_max3_f32 v153, v153, v94, v95
	v_max3_f32 v152, v152, v60, v61
	v_max3_f32 v153, v153, v62, v63
	v_mfma_f32_32x32x16_bf16 a[64:79], v[148:151], v[128:131], a[64:79]
	ds_read_b128 a[236:239], v221 offset:8192
	v_max3_f32 v154, v64, v65, v32
	v_max3_f32 v155, v66, v67, v33
	v_max3_f32 v154, v154, v34, v35
	v_mfma_f32_32x32x16_bf16 a[80:95], v[148:151], v[144:147], a[80:95]
	ds_read_b128 a[240:243], v218 offset:8320
	v_max3_f32 v148, v154, v68, v69
	v_max3_f32 v149, v155, v70, v71
	v_max3_f32 v148, v148, v36, v37
	v_max3_f32 v149, v149, v38, v39
	v_mfma_f32_32x32x16_bf16 a[96:111], v[136:139], v[128:131], a[96:111]
	ds_read_b128 a[244:247], v219 offset:8320
	v_max3_f32 v128, v148, v72, v73
	v_max3_f32 v129, v149, v74, v75
	v_max3_f32 v128, v128, v40, v41
	v_max3_f32 v129, v129, v42, v43
	v_mfma_f32_32x32x16_bf16 a[112:127], v[136:139], v[144:147], a[112:127]
	ds_read_b128 a[248:251], v220 offset:8320
	v_max3_f32 v128, v128, v76, v77
	v_max3_f32 v129, v129, v78, v79
	v_max3_f32 v128, v128, v44, v45
	v_max3_f32 v130, v129, v46, v47
	v_mfma_f32_32x32x16_bf16 a[0:15], v[132:135], v[112:115], a[0:15]
	ds_read_b128 a[252:255], v221 offset:8320
	v_max_f32_e32 v129, v152, v153
	v_mov_b32_e32 v131, v129
	s_nop 1
	v_permlane32_swap_b32_e32 v129, v131
	v_max_f32_e32 v129, v129, v131
	v_mfma_f32_32x32x16_bf16 a[16:31], v[132:135], v[140:143], a[16:31]
	v_max_f32_e32 v128, v128, v130
	v_mov_b32_e32 v130, v128
	s_nop 1
	v_permlane32_swap_b32_e32 v128, v130
	v_max_f32_e32 v128, v128, v130
	v_max_f32_e32 v130, v129, v129
	v_max_f32_e32 v131, v128, v128
	v_max_f32_e32 v130, v130, v131
	s_mov_b32 s0, 0x41000000
	v_mfma_f32_32x32x16_bf16 a[32:47], v[124:127], v[112:115], a[32:47]
	v_cmp_lt_f32_e32 vcc, s0, v130
	s_cmp_lg_u64 vcc, 0
	s_cselect_b64 s[0:1], -1, 0
	s_cbranch_vccnz .LBB0_41
	v_mov_b32_e32 v216, 1.0

.LBB0_17:
	v_exp_f32_e32 v48, v48
	v_exp_f32_e32 v49, v49
	v_mfma_f32_32x32x16_bf16 v[112:127], a[192:195], a[128:131], v[0:15]
	ds_read_b64_tr_b16 v[172:173], v215 offset:0
	v_cvt_pk_bf16_f32 v164, v128, v129
	v_exp_f32_e32 v50, v50
	v_exp_f32_e32 v51, v51
	v_mfma_f32_32x32x16_bf16 v[96:111], a[192:195], a[160:163], v[16:31]
	ds_read_b64_tr_b16 v[174:175], v215 offset:0x800
	v_cvt_pk_bf16_f32 v165, v130, v131
	v_mfma_f32_32x32x16_bf16 v[80:95], a[224:227], a[128:131], v[0:15]
	ds_read_b64_tr_b16 v[184:185], v215 offset:0x200
	v_exp_f32_e32 v239, v52
	v_exp_f32_e32 v240, v53
	v_cvt_pk_bf16_f32 v166, v132, v133
	v_mfma_f32_32x32x16_bf16 v[64:79], a[224:227], a[160:163], v[16:31]
	ds_read_b64_tr_b16 v[186:187], v215 offset:0xa00
	ds_read_b64_tr_b16 v[180:181], v215 offset:0x400
	v_exp_f32_e32 v241, v54
	v_exp_f32_e32 v242, v55
	v_cvt_pk_bf16_f32 v167, v134, v135
	v_exp_f32_e32 v227, v56
	v_exp_f32_e32 v228, v57
	v_mfma_f32_32x32x16_bf16 v[112:127], a[196:199], a[132:135], v[112:127]
	ds_read_b64_tr_b16 v[182:183], v215 offset:0xc00
	v_cvt_pk_bf16_f32 v128, v136, v137
	v_exp_f32_e32 v229, v58
	v_exp_f32_e32 v230, v59
	v_mfma_f32_32x32x16_bf16 v[96:111], a[196:199], a[164:167], v[96:111]
	ds_read_b64_tr_b16 v[188:189], v215 offset:0x600
	v_cvt_pk_bf16_f32 v129, v138, v139
	v_exp_f32_e32 v231, v60
	v_exp_f32_e32 v232, v61
	v_mfma_f32_32x32x16_bf16 v[80:95], a[228:231], a[132:135], v[80:95]
	ds_read_b64_tr_b16 v[190:191], v215 offset:0xe00
	v_cvt_pk_bf16_f32 v130, v140, v141
	v_mfma_f32_32x32x16_bf16 v[64:79], a[228:231], a[164:167], v[64:79]
	ds_read_b64_tr_b16 v[176:177], v215 offset:0x1000
	v_exp_f32_e32 v233, v62
	v_exp_f32_e32 v234, v63
	ds_read_b64_tr_b16 v[178:179], v215 offset:0x1800
	v_cvt_pk_bf16_f32 v131, v142, v143
	v_exp_f32_e32 v141, v32
	v_exp_f32_e32 v142, v33
	v_mfma_f32_32x32x16_bf16 v[112:127], a[200:203], a[136:139], v[112:127]
	ds_read_b64_tr_b16 v[168:169], v215 offset:0x1200
	v_cvt_pk_bf16_f32 v192, v144, v145
	v_exp_f32_e32 v143, v34
	v_mfma_f32_32x32x16_bf16 v[96:111], a[200:203], a[168:171], v[96:111]
	ds_read_b64_tr_b16 v[170:171], v215 offset:0x1a00
	v_exp_f32_e32 v243, v35
	v_cvt_pk_bf16_f32 v193, v146, v147
	v_mfma_f32_32x32x16_bf16 v[80:95], a[232:235], a[136:139], v[80:95]
	ds_read_b64_tr_b16 v[160:161], v215 offset:0x1400
	v_exp_f32_e32 v244, v36
	v_exp_f32_e32 v245, v37
	v_cvt_pk_bf16_f32 v194, v148, v149
	v_mfma_f32_32x32x16_bf16 v[64:79], a[232:235], a[168:171], v[64:79]
	ds_read_b64_tr_b16 v[162:163], v215 offset:0x1c00
	ds_read_b64_tr_b16 v[136:137], v215 offset:0x1600
	v_exp_f32_e32 v246, v38
	v_exp_f32_e32 v247, v39
	v_cvt_pk_bf16_f32 v195, v150, v151
	v_exp_f32_e32 v148, v40
	v_exp_f32_e32 v149, v41
	v_mfma_f32_32x32x16_bf16 v[112:127], a[204:207], a[140:143], v[112:127]
	ds_read_b64_tr_b16 v[138:139], v215 offset:0x1e00
	v_cvt_pk_bf16_f32 v144, v152, v153
	v_exp_f32_e32 v150, v42
	v_exp_f32_e32 v151, v43
	v_mfma_f32_32x32x16_bf16 v[96:111], a[204:207], a[172:175], v[96:111]
	ds_read_b64_tr_b16 v[132:133], v215 offset:0x2000
	v_cvt_pk_bf16_f32 v145, v154, v155
	v_exp_f32_e32 v152, v44
	v_exp_f32_e32 v153, v45
	v_mfma_f32_32x32x16_bf16 v[80:95], a[236:239], a[140:143], v[80:95]
	ds_read_b64_tr_b16 v[134:135], v215 offset:0x2800
	v_cvt_pk_bf16_f32 v146, v156, v157
	v_mfma_f32_32x32x16_bf16 v[64:79], a[236:239], a[172:175], v[64:79]
	ds_read_b64_tr_b16 v[60:61], v215 offset:0x2200
	v_exp_f32_e32 v154, v46
	v_exp_f32_e32 v155, v47
	ds_read_b64_tr_b16 v[62:63], v215 offset:0x2a00
	v_cvt_pk_bf16_f32 v147, v158, v159
	s_mov_b32 s0, s29
	v_mfma_f32_32x32x16_bf16 v[112:127], a[208:211], a[144:147], v[112:127]
	ds_read_b64_tr_b16 v[56:57], v215 offset:0x2400
	v_cvt_pk_bf16_f32 v52, v48, v49
	v_add_f32_e32 v32, v236, v48
	v_add_f32_e32 v33, v235, v49
	s_add_i32 s57, s58, s59
	s_and_b32 s57, s57, 0x7ffff
	s_mov_b32 s33, s57
	s_mov_b32 s1, s33
	v_mfma_f32_32x32x16_bf16 v[96:111], a[208:211], a[176:179], v[96:111]
	ds_read_b64_tr_b16 v[58:59], v215 offset:0x2c00
	v_cvt_pk_bf16_f32 v53, v50, v51
	v_add_f32_e32 v32, v32, v50
	v_add_f32_e32 v33, v33, v51
	s_mov_b32 s35, s20
	v_mfma_f32_32x32x16_bf16 v[80:95], a[240:243], a[144:147], v[80:95]
	ds_read_b64_tr_b16 v[48:49], v215 offset:0x2600
	v_cvt_pk_bf16_f32 v54, v239, v240
	v_add_f32_e32 v32, v32, v239
	v_add_f32_e32 v33, v33, v240
	s_add_i32 s36, s57, 0x400
	v_mfma_f32_32x32x16_bf16 v[64:79], a[240:243], a[176:179], v[64:79]
	ds_read_b64_tr_b16 v[50:51], v215 offset:0x2e00
	ds_read_b64_tr_b16 v[44:45], v215 offset:0x3000
	v_cvt_pk_bf16_f32 v55, v241, v242
	v_add_f32_e32 v32, v32, v241
	v_add_f32_e32 v33, v33, v242
	s_mov_b32 s37, s21
	v_mfma_f32_32x32x16_bf16 v[112:127], a[212:215], a[148:151], v[112:127]
	ds_read_b64_tr_b16 v[46:47], v215 offset:0x3800
	v_add_f32_e32 v32, v32, v227
	v_add_f32_e32 v33, v33, v228
	s_add_i32 s34, s57, 0x800
	s_mov_b32 s38, s34
	v_mfma_f32_32x32x16_bf16 v[96:111], a[212:215], a[180:183], v[96:111]
	ds_read_b64_tr_b16 v[40:41], v215 offset:0x3200
	v_add_f32_e32 v32, v32, v229
	v_add_f32_e32 v33, v33, v230
	s_mov_b32 s39, s22
	v_mfma_f32_32x32x16_bf16 v[80:95], a[244:247], a[148:151], v[80:95]
	ds_read_b64_tr_b16 v[42:43], v215 offset:0x3a00
	v_add_f32_e32 v32, v32, v231
	v_add_f32_e32 v33, v33, v232
	s_add_i32 s40, s57, 0xc00
	v_mfma_f32_32x32x16_bf16 v[64:79], a[244:247], a[180:183], v[64:79]
	ds_read_b64_tr_b16 v[36:37], v215 offset:0x3400
	ds_read_b64_tr_b16 v[38:39], v215 offset:0x3c00
	v_add_f32_e32 v156, v32, v233
	v_add_f32_e32 v157, v33, v234
	s_mov_b32 s41, s23
	v_mfma_f32_32x32x16_bf16 v[112:127], a[216:219], a[152:155], v[112:127]
	ds_read_b64_tr_b16 v[32:33], v215 offset:0x3600
	v_cvt_pk_bf16_f32 v140, v141, v142
	v_add_f32_e32 v158, v237, v141
	v_add_f32_e32 v142, v238, v142
	s_mov_b32 s42, s58
	v_mfma_f32_32x32x16_bf16 v[96:111], a[216:219], a[184:187], v[96:111]
	ds_read_b64_tr_b16 v[34:35], v215 offset:0x3e00
	v_cvt_pk_bf16_f32 v141, v143, v243
	v_add_f32_e32 v143, v158, v143
	v_add_f32_e32 v158, v142, v243
	v_mfma_f32_32x32x16_bf16 v[80:95], a[248:251], a[152:155], v[80:95]
	s_mov_b32 s43, s24
	v_cvt_pk_bf16_f32 v142, v244, v245
	v_add_f32_e32 v159, v143, v244
	v_add_f32_e32 v158, v158, v245
	v_mfma_f32_32x32x16_bf16 v[64:79], a[248:251], a[184:187], v[64:79]
	s_add_i32 s44, s58, 0x80
	v_cvt_pk_bf16_f32 v143, v246, v247
	v_add_f32_e32 v159, v159, v246
	v_add_f32_e32 v158, v158, v247
	v_mfma_f32_32x32x16_bf16 v[112:127], a[220:223], a[156:159], v[112:127]
	s_mov_b32 s45, s25
	v_add_f32_e32 v159, v159, v148
	v_add_f32_e32 v158, v158, v149
	v_mfma_f32_32x32x16_bf16 v[96:111], a[220:223], a[188:191], v[96:111]
	s_add_i32 s46, s58, 0x800
	v_add_f32_e32 v159, v159, v150
	v_add_f32_e32 v158, v158, v151
	v_mfma_f32_32x32x16_bf16 v[80:95], a[252:255], a[156:159], v[80:95]
	s_mov_b32 s47, s26
	v_add_f32_e32 v159, v159, v152
	v_add_f32_e32 v158, v158, v153
	v_mfma_f32_32x32x16_bf16 v[64:79], a[252:255], a[188:191], v[64:79]
	s_add_i32 s48, s58, 0x880
	v_add_f32_e32 v159, v159, v154
	v_add_f32_e32 v158, v158, v155
	s_nop 0
	s_nop 4
	v_add_f32_e32 v156, v156, v157
	s_waitcnt vmcnt(0) lgkmcnt(0)
	s_barrier
	v_mfma_f32_32x32x16_bf16 a[0:15], v[172:175], v[164:167], a[0:15]
	v_mov_b32_e32 v157, v156
	s_mov_b32 m0, s0
	s_nop 0
	buffer_load_dwordx4 v222, s[12:15], s1 offen lds
	v_mfma_f32_32x32x16_bf16 a[16:31], v[172:175], v[192:195], a[16:31]
	v_permlane32_swap_b32_e32 v156, v157
	v_add_f32_e32 v156, v156, v157
	s_mov_b32 m0, s35
	s_nop 0
	buffer_load_dwordx4 v223, s[12:15], s36 offen lds
	ds_read_b128 a[192:195], v217 offset:0
	v_mfma_f32_32x32x16_bf16 a[32:47], v[184:187], v[164:167], a[32:47]
	v_add_f32_e32 v225, v225, v156
	v_add_f32_e32 v156, v159, v158
	v_mov_b32_e32 v157, v156
	s_mov_b32 m0, s37
	s_nop 0
	buffer_load_dwordx4 v222, s[12:15], s38 offen lds
	ds_read_b128 a[196:199], v199 offset:0
	v_mfma_f32_32x32x16_bf16 a[48:63], v[184:187], v[192:195], a[48:63]
	v_permlane32_swap_b32_e32 v156, v157
	v_add_f32_e32 v156, v156, v157
	s_mov_b32 m0, s39
	s_nop 0
	buffer_load_dwordx4 v223, s[12:15], s40 offen lds
	ds_read_b128 a[200:203], v198 offset:0
	v_mfma_f32_32x32x16_bf16 a[64:79], v[180:183], v[164:167], a[64:79]
	v_add_f32_e32 v226, v226, v156
	s_mov_b32 m0, s41
	s_nop 0
	buffer_load_dwordx4 v196, s[4:7], s42 offen lds
	ds_read_b128 a[204:207], v197 offset:0
	v_mfma_f32_32x32x16_bf16 a[80:95], v[180:183], v[192:195], a[80:95]
	s_mov_b32 m0, s43
	s_nop 0
	buffer_load_dwordx4 v196, s[4:7], s44 offen lds
	ds_read_b128 a[208:211], v217 offset:128
	v_mfma_f32_32x32x16_bf16 a[96:111], v[188:191], v[164:167], a[96:111]
	s_mov_b32 m0, s45
	s_nop 0
	buffer_load_dwordx4 v196, s[4:7], s46 offen lds
	ds_read_b128 a[212:215], v199 offset:128
	v_mfma_f32_32x32x16_bf16 a[112:127], v[188:191], v[192:195], a[112:127]
	s_mov_b32 m0, s47
	s_nop 0
	buffer_load_dwordx4 v196, s[4:7], s48 offen lds
	ds_read_b128 a[216:219], v198 offset:128
	s_nop 0
	v_mfma_f32_32x32x16_bf16 a[0:15], v[176:179], v[128:131], a[0:15]
	ds_read_b128 a[220:223], v197 offset:128
	s_cmp_gt_u32 s27, 12
	s_cbranch_scc1 .Lkc_skip_a
	v_cvt_pk_bf16_f32 v248, v248, v249
	v_cvt_pk_bf16_f32 v249, v250, v251
	v_cvt_pk_bf16_f32 v250, v252, v253
	v_cvt_pk_bf16_f32 v251, v254, v255
	v_lshrrev_b32_e32 v252, 1, v208
	buffer_store_dwordx4 v[248:251], v252, s[12:15], s56 offen sc1
	s_nop 1
	global_load_dwordx4 v[248:251], v208, s[74:75] nt
	global_load_dwordx4 v[252:255], v208, s[74:75] offset:16 nt
	s_add_u32 s74, s74, 0x2000
	s_addc_u32 s75, s75, 0

.LBB0_19:
	s_waitcnt lgkmcnt(0)
	v_exp_f32_e32 v80, v80
	v_exp_f32_e32 v81, v81
	v_mfma_f32_32x32x16_bf16 v[112:127], a[192:195], a[128:131], v[0:15]
	ds_read_b64_tr_b16 v[180:181], v212 offset:0
	v_cvt_pk_bf16_f32 v168, v128, v129
	v_exp_f32_e32 v82, v82
	v_exp_f32_e32 v83, v83
	v_mfma_f32_32x32x16_bf16 v[96:111], a[192:195], a[160:163], v[16:31]
	ds_read_b64_tr_b16 v[182:183], v212 offset:0x800
	v_cvt_pk_bf16_f32 v169, v130, v131
	v_mfma_f32_32x32x16_bf16 v[48:63], a[224:227], a[128:131], v[0:15]
	ds_read_b64_tr_b16 v[184:185], v212 offset:0x200
	v_exp_f32_e32 v239, v84
	v_exp_f32_e32 v240, v85
	v_cvt_pk_bf16_f32 v170, v132, v133
	v_mfma_f32_32x32x16_bf16 v[32:47], a[224:227], a[160:163], v[16:31]
	ds_read_b64_tr_b16 v[186:187], v212 offset:0xa00
	ds_read_b64_tr_b16 v[176:177], v212 offset:0x400
	v_exp_f32_e32 v241, v86
	v_exp_f32_e32 v242, v87
	v_cvt_pk_bf16_f32 v171, v134, v135
	v_exp_f32_e32 v227, v88
	v_exp_f32_e32 v228, v89
	v_mfma_f32_32x32x16_bf16 v[112:127], a[196:199], a[132:135], v[112:127]
	ds_read_b64_tr_b16 v[178:179], v212 offset:0xc00
	v_cvt_pk_bf16_f32 v128, v136, v137
	v_exp_f32_e32 v229, v90
	v_exp_f32_e32 v230, v91
	v_mfma_f32_32x32x16_bf16 v[96:111], a[196:199], a[164:167], v[96:111]
	ds_read_b64_tr_b16 v[188:189], v212 offset:0x600
	v_cvt_pk_bf16_f32 v129, v138, v139
	v_exp_f32_e32 v231, v92
	v_exp_f32_e32 v232, v93
	v_mfma_f32_32x32x16_bf16 v[48:63], a[228:231], a[132:135], v[48:63]
	ds_read_b64_tr_b16 v[190:191], v212 offset:0xe00
	v_cvt_pk_bf16_f32 v130, v140, v141
	v_mfma_f32_32x32x16_bf16 v[32:47], a[228:231], a[164:167], v[32:47]
	ds_read_b64_tr_b16 v[172:173], v212 offset:0x1000
	v_exp_f32_e32 v233, v94
	v_exp_f32_e32 v234, v95
	ds_read_b64_tr_b16 v[174:175], v212 offset:0x1800
	v_cvt_pk_bf16_f32 v131, v142, v143
	v_exp_f32_e32 v141, v64
	v_exp_f32_e32 v142, v65
	v_mfma_f32_32x32x16_bf16 v[112:127], a[200:203], a[136:139], v[112:127]
	ds_read_b64_tr_b16 v[164:165], v212 offset:0x1200
	v_cvt_pk_bf16_f32 v192, v144, v145
	v_exp_f32_e32 v143, v66
	v_mfma_f32_32x32x16_bf16 v[96:111], a[200:203], a[168:171], v[96:111]
	ds_read_b64_tr_b16 v[166:167], v212 offset:0x1a00
	v_exp_f32_e32 v243, v67
	v_cvt_pk_bf16_f32 v193, v146, v147
	v_mfma_f32_32x32x16_bf16 v[48:63], a[232:235], a[136:139], v[48:63]
	ds_read_b64_tr_b16 v[160:161], v212 offset:0x1400
	v_exp_f32_e32 v244, v68
	v_exp_f32_e32 v245, v69
	v_cvt_pk_bf16_f32 v194, v148, v149
	v_mfma_f32_32x32x16_bf16 v[32:47], a[232:235], a[168:171], v[32:47]
	ds_read_b64_tr_b16 v[162:163], v212 offset:0x1c00
	ds_read_b64_tr_b16 v[136:137], v212 offset:0x1600
	v_exp_f32_e32 v246, v70
	v_exp_f32_e32 v247, v71
	v_cvt_pk_bf16_f32 v195, v150, v151
	v_exp_f32_e32 v148, v72
	v_exp_f32_e32 v149, v73
	v_mfma_f32_32x32x16_bf16 v[112:127], a[204:207], a[140:143], v[112:127]
	ds_read_b64_tr_b16 v[138:139], v212 offset:0x1e00
	v_cvt_pk_bf16_f32 v144, v152, v153
	v_exp_f32_e32 v150, v74
	v_exp_f32_e32 v151, v75
	v_mfma_f32_32x32x16_bf16 v[96:111], a[204:207], a[172:175], v[96:111]
	ds_read_b64_tr_b16 v[132:133], v212 offset:0x2000
	v_cvt_pk_bf16_f32 v145, v154, v155
	v_exp_f32_e32 v152, v76
	v_exp_f32_e32 v153, v77
	v_mfma_f32_32x32x16_bf16 v[48:63], a[236:239], a[140:143], v[48:63]
	ds_read_b64_tr_b16 v[134:135], v212 offset:0x2800
	v_cvt_pk_bf16_f32 v146, v156, v157
	v_mfma_f32_32x32x16_bf16 v[32:47], a[236:239], a[172:175], v[32:47]
	ds_read_b64_tr_b16 v[92:93], v212 offset:0x2200
	v_exp_f32_e32 v154, v78
	v_exp_f32_e32 v155, v79
	ds_read_b64_tr_b16 v[94:95], v212 offset:0x2a00
	v_cvt_pk_bf16_f32 v147, v158, v159
	s_mov_b32 s0, s3
	v_mfma_f32_32x32x16_bf16 v[112:127], a[208:211], a[144:147], v[112:127]
	ds_read_b64_tr_b16 v[88:89], v212 offset:0x2400
	v_cvt_pk_bf16_f32 v84, v80, v81
	v_add_f32_e32 v64, v236, v80
	v_add_f32_e32 v65, v235, v81
	s_add_i32 s58, s57, s60
	s_and_b32 s58, s58, 0x7ffff
	s_mov_b32 s1, s58
	v_mfma_f32_32x32x16_bf16 v[96:111], a[208:211], a[176:179], v[96:111]
	ds_read_b64_tr_b16 v[90:91], v212 offset:0x2c00
	v_cvt_pk_bf16_f32 v85, v82, v83
	v_add_f32_e32 v64, v64, v82
	v_add_f32_e32 v65, v65, v83
	s_mov_b32 s35, s10
	v_mfma_f32_32x32x16_bf16 v[48:63], a[240:243], a[144:147], v[48:63]
	ds_read_b64_tr_b16 v[80:81], v212 offset:0x2600
	v_cvt_pk_bf16_f32 v86, v239, v240
	v_add_f32_e32 v64, v64, v239
	v_add_f32_e32 v65, v65, v240
	s_add_i32 s36, s58, 0x400
	v_mfma_f32_32x32x16_bf16 v[32:47], a[240:243], a[176:179], v[32:47]
	ds_read_b64_tr_b16 v[82:83], v212 offset:0x2e00
	ds_read_b64_tr_b16 v[76:77], v212 offset:0x3000
	v_cvt_pk_bf16_f32 v87, v241, v242
	v_add_f32_e32 v64, v64, v241
	v_add_f32_e32 v65, v65, v242
	s_mov_b32 s37, s11
	v_mfma_f32_32x32x16_bf16 v[112:127], a[212:215], a[148:151], v[112:127]
	ds_read_b64_tr_b16 v[78:79], v212 offset:0x3800
	v_add_f32_e32 v64, v64, v227
	v_add_f32_e32 v65, v65, v228
	s_add_i32 s38, s58, 0x800
	v_mfma_f32_32x32x16_bf16 v[96:111], a[212:215], a[180:183], v[96:111]
	ds_read_b64_tr_b16 v[72:73], v212 offset:0x3200
	v_add_f32_e32 v64, v64, v229
	v_add_f32_e32 v65, v65, v230
	s_mov_b32 s39, s16
	v_mfma_f32_32x32x16_bf16 v[48:63], a[244:247], a[148:151], v[48:63]
	ds_read_b64_tr_b16 v[74:75], v212 offset:0x3a00
	v_add_f32_e32 v64, v64, v231
	v_add_f32_e32 v65, v65, v232
	s_add_i32 s40, s58, 0xc00
	v_mfma_f32_32x32x16_bf16 v[32:47], a[244:247], a[180:183], v[32:47]
	ds_read_b64_tr_b16 v[68:69], v212 offset:0x3400
	ds_read_b64_tr_b16 v[70:71], v212 offset:0x3c00
	v_add_f32_e32 v156, v64, v233
	v_add_f32_e32 v157, v65, v234
	s_mov_b32 s41, s2
	v_mfma_f32_32x32x16_bf16 v[112:127], a[216:219], a[152:155], v[112:127]
	ds_read_b64_tr_b16 v[64:65], v212 offset:0x3600
	v_cvt_pk_bf16_f32 v140, v141, v142
	v_add_f32_e32 v158, v237, v141
	v_add_f32_e32 v142, v238, v142
	v_mfma_f32_32x32x16_bf16 v[96:111], a[216:219], a[184:187], v[96:111]
	ds_read_b64_tr_b16 v[66:67], v212 offset:0x3e00
	v_cvt_pk_bf16_f32 v141, v143, v243
	v_add_f32_e32 v143, v158, v143
	v_add_f32_e32 v158, v142, v243
	v_mfma_f32_32x32x16_bf16 v[48:63], a[248:251], a[152:155], v[48:63]
	s_mov_b32 s42, s17
	v_cvt_pk_bf16_f32 v142, v244, v245
	v_add_f32_e32 v159, v143, v244
	v_add_f32_e32 v158, v158, v245
	v_mfma_f32_32x32x16_bf16 v[32:47], a[248:251], a[184:187], v[32:47]
	s_add_i32 s43, s57, 0x80
	v_cvt_pk_bf16_f32 v143, v246, v247
	v_add_f32_e32 v159, v159, v246
	v_add_f32_e32 v158, v158, v247
	v_mfma_f32_32x32x16_bf16 v[112:127], a[220:223], a[156:159], v[112:127]
	s_mov_b32 s44, s18
	v_add_f32_e32 v159, v159, v148
	v_add_f32_e32 v158, v158, v149
	v_mfma_f32_32x32x16_bf16 v[96:111], a[220:223], a[188:191], v[96:111]
	v_add_f32_e32 v159, v159, v150
	v_add_f32_e32 v158, v158, v151
	v_mfma_f32_32x32x16_bf16 v[48:63], a[252:255], a[156:159], v[48:63]
	s_mov_b32 s45, s19
	v_add_f32_e32 v159, v159, v152
	v_add_f32_e32 v158, v158, v153
	v_mfma_f32_32x32x16_bf16 v[32:47], a[252:255], a[188:191], v[32:47]
	s_add_i32 s46, s57, 0x880
	v_add_f32_e32 v159, v159, v154
	v_add_f32_e32 v158, v158, v155
	s_nop 0
	s_nop 4
	v_add_f32_e32 v156, v156, v157
	s_waitcnt vmcnt(0) lgkmcnt(0)
	s_barrier
	v_mfma_f32_32x32x16_bf16 a[0:15], v[180:183], v[168:171], a[0:15]
	v_mov_b32_e32 v157, v156
	s_mov_b32 m0, s0
	s_nop 0
	buffer_load_dwordx4 v222, s[12:15], s1 offen lds
	v_mfma_f32_32x32x16_bf16 a[16:31], v[180:183], v[192:195], a[16:31]
	v_permlane32_swap_b32_e32 v156, v157
	v_add_f32_e32 v156, v156, v157
	s_mov_b32 m0, s35
	s_nop 0
	buffer_load_dwordx4 v223, s[12:15], s36 offen lds
	ds_read_b128 a[192:195], v218 offset:0
	v_mfma_f32_32x32x16_bf16 a[32:47], v[184:187], v[168:171], a[32:47]
	v_add_f32_e32 v225, v225, v156
	v_add_f32_e32 v156, v159, v158
	v_mov_b32_e32 v157, v156
	s_mov_b32 m0, s37
	s_nop 0
	buffer_load_dwordx4 v222, s[12:15], s38 offen lds
	ds_read_b128 a[196:199], v219 offset:0
	v_mfma_f32_32x32x16_bf16 a[48:63], v[184:187], v[192:195], a[48:63]
	v_permlane32_swap_b32_e32 v156, v157
	v_add_f32_e32 v156, v156, v157
	s_mov_b32 m0, s39
	s_nop 0
	buffer_load_dwordx4 v223, s[12:15], s40 offen lds
	ds_read_b128 a[200:203], v220 offset:0
	v_mfma_f32_32x32x16_bf16 a[64:79], v[176:179], v[168:171], a[64:79]
	v_add_f32_e32 v226, v226, v156
	s_mov_b32 m0, s41
	s_nop 0
	buffer_load_dwordx4 v196, s[4:7], s33 offen lds
	ds_read_b128 a[204:207], v221 offset:0
	v_mfma_f32_32x32x16_bf16 a[80:95], v[176:179], v[192:195], a[80:95]
	s_mov_b32 m0, s42
	s_nop 0
	buffer_load_dwordx4 v196, s[4:7], s43 offen lds
	ds_read_b128 a[208:211], v218 offset:128
	v_mfma_f32_32x32x16_bf16 a[96:111], v[188:191], v[168:171], a[96:111]
	s_mov_b32 m0, s44
	s_nop 0
	buffer_load_dwordx4 v196, s[4:7], s34 offen lds
	ds_read_b128 a[212:215], v219 offset:128
	v_mfma_f32_32x32x16_bf16 a[112:127], v[188:191], v[192:195], a[112:127]
	s_mov_b32 m0, s45
	s_nop 0
	buffer_load_dwordx4 v196, s[4:7], s46 offen lds
	ds_read_b128 a[216:219], v220 offset:128
	s_nop 0
	v_mfma_f32_32x32x16_bf16 a[0:15], v[172:175], v[128:131], a[0:15]
	ds_read_b128 a[220:223], v221 offset:128
	s_cmp_gt_u32 s27, 12
	s_cbranch_scc1 .Lkc_skip_b
	v_pk_add_f32 v[200:201], v[248:249], v[200:201]
	v_pk_add_f32 v[202:203], v[250:251], v[202:203]
	v_pk_add_f32 v[204:205], v[252:253], v[204:205]
	v_pk_add_f32 v[206:207], v[254:255], v[206:207]
	v_cvt_pk_bf16_f32 v248, v248, v249
	v_cvt_pk_bf16_f32 v249, v250, v251
	v_cvt_pk_bf16_f32 v250, v252, v253
	v_cvt_pk_bf16_f32 v251, v254, v255
	v_lshrrev_b32_e32 v252, 1, v208
	buffer_store_dwordx4 v[248:251], v252, s[4:7], s56 offen sc1
	s_add_i32 s56, s56, 0x1000
	s_cmp_gt_u32 s27, 10
	s_cbranch_scc1 .Lkc_skip_b
	s_nop 1
	global_load_dwordx4 v[248:251], v208, s[54:55] nt
	global_load_dwordx4 v[252:255], v208, s[54:55] offset:16 nt
	s_add_u32 s54, s54, 0x2000
	s_addc_u32 s55, s55, 0

.LBB0_36:
	s_lshl_b32 s53, s50, 6
	s_add_i32 s53, s53, s52
	v_mov_b32_e32 v200, s53
	s_lshl_b32 s53, s50, 14
	s_add_i32 s53, s53, 0x10000
	v_mov_b32_e32 v201, s53
	v_mbcnt_lo_u32_b32 v204, -1, 0
	v_mbcnt_hi_u32_b32 v204, -1, v204
	v_lshrrev_b32_e32 v202, 4, v204
	v_add_u32_e32 v203, 4, v202
	v_add_u32_e32 v205, 8, v202
	v_add_u32_e32 v206, 12, v202
	v_add_u32_e32 v207, 16, v202
	v_add_u32_e32 v208, 20, v202
	v_add_u32_e32 v209, 24, v202
	v_add_u32_e32 v210, 28, v202
	v_exp_f32_e32 v48, v48
	v_exp_f32_e32 v49, v49
	v_mfma_f32_32x32x16_bf16 v[112:127], a[192:195], a[128:131], v[0:15]
	ds_read_b64_tr_b16 v[180:181], v215 offset:0
	v_cvt_pk_bf16_f32 v164, v128, v129
	v_exp_f32_e32 v50, v50
	v_exp_f32_e32 v51, v51
	v_mfma_f32_32x32x16_bf16 v[96:111], a[192:195], a[160:163], v[16:31]
	ds_read_b64_tr_b16 v[182:183], v215 offset:0x800
	v_cvt_pk_bf16_f32 v165, v130, v131
	v_exp_f32_e32 v218, v52
	v_exp_f32_e32 v219, v53
	v_mfma_f32_32x32x16_bf16 v[80:95], a[224:227], a[128:131], v[0:15]
	ds_read_b64_tr_b16 v[188:189], v215 offset:0x200
	v_cvt_pk_bf16_f32 v166, v132, v133
	v_mfma_f32_32x32x16_bf16 v[64:79], a[224:227], a[160:163], v[16:31]
	ds_read_b64_tr_b16 v[190:191], v215 offset:0xa00
	ds_read_b64_tr_b16 v[176:177], v215 offset:0x400
	v_exp_f32_e32 v230, v54
	v_exp_f32_e32 v231, v55
	v_cvt_pk_bf16_f32 v167, v134, v135
	v_exp_f32_e32 v220, v56
	v_exp_f32_e32 v221, v57
	v_mfma_f32_32x32x16_bf16 v[112:127], a[196:199], a[132:135], v[112:127]
	ds_read_b64_tr_b16 v[178:179], v215 offset:0xc00
	v_cvt_pk_bf16_f32 v128, v136, v137
	v_exp_f32_e32 v222, v58
	v_exp_f32_e32 v223, v59
	v_mfma_f32_32x32x16_bf16 v[96:111], a[196:199], a[164:167], v[96:111]
	ds_read_b64_tr_b16 v[184:185], v215 offset:0x600
	v_cvt_pk_bf16_f32 v129, v138, v139
	v_exp_f32_e32 v224, v60
	v_exp_f32_e32 v227, v61
	v_mfma_f32_32x32x16_bf16 v[80:95], a[228:231], a[132:135], v[80:95]
	ds_read_b64_tr_b16 v[186:187], v215 offset:0xe00
	v_cvt_pk_bf16_f32 v130, v140, v141
	v_mfma_f32_32x32x16_bf16 v[64:79], a[228:231], a[164:167], v[64:79]
	ds_read_b64_tr_b16 v[172:173], v215 offset:0x1000
	v_exp_f32_e32 v228, v62
	v_exp_f32_e32 v229, v63
	ds_read_b64_tr_b16 v[174:175], v215 offset:0x1800
	v_cvt_pk_bf16_f32 v131, v142, v143
	v_exp_f32_e32 v141, v32
	v_exp_f32_e32 v142, v33
	v_mfma_f32_32x32x16_bf16 v[112:127], a[200:203], a[136:139], v[112:127]
	ds_read_b64_tr_b16 v[168:169], v215 offset:0x1200
	v_cvt_pk_bf16_f32 v192, v144, v145
	v_exp_f32_e32 v143, v34
	v_mfma_f32_32x32x16_bf16 v[96:111], a[200:203], a[168:171], v[96:111]
	ds_read_b64_tr_b16 v[170:171], v215 offset:0x1a00
	v_exp_f32_e32 v232, v35
	v_cvt_pk_bf16_f32 v193, v146, v147
	v_mfma_f32_32x32x16_bf16 v[80:95], a[232:235], a[136:139], v[80:95]
	ds_read_b64_tr_b16 v[160:161], v215 offset:0x1400
	v_exp_f32_e32 v233, v36
	v_exp_f32_e32 v234, v37
	v_cvt_pk_bf16_f32 v194, v148, v149
	v_mfma_f32_32x32x16_bf16 v[64:79], a[232:235], a[168:171], v[64:79]
	ds_read_b64_tr_b16 v[162:163], v215 offset:0x1c00
	ds_read_b64_tr_b16 v[136:137], v215 offset:0x1600
	v_exp_f32_e32 v239, v38
	v_exp_f32_e32 v240, v39
	v_cvt_pk_bf16_f32 v195, v150, v151
	v_exp_f32_e32 v148, v40
	v_exp_f32_e32 v149, v41
	v_mfma_f32_32x32x16_bf16 v[112:127], a[204:207], a[140:143], v[112:127]
	ds_read_b64_tr_b16 v[138:139], v215 offset:0x1e00
	v_cvt_pk_bf16_f32 v144, v152, v153
	v_exp_f32_e32 v150, v42
	v_exp_f32_e32 v151, v43
	v_mfma_f32_32x32x16_bf16 v[96:111], a[204:207], a[172:175], v[96:111]
	ds_read_b64_tr_b16 v[132:133], v215 offset:0x2000
	v_cvt_pk_bf16_f32 v145, v154, v155
	v_exp_f32_e32 v152, v44
	v_exp_f32_e32 v153, v45
	v_mfma_f32_32x32x16_bf16 v[80:95], a[236:239], a[140:143], v[80:95]
	ds_read_b64_tr_b16 v[134:135], v215 offset:0x2800
	v_cvt_pk_bf16_f32 v146, v156, v157
	v_mfma_f32_32x32x16_bf16 v[64:79], a[236:239], a[172:175], v[64:79]
	ds_read_b64_tr_b16 v[60:61], v215 offset:0x2200
	v_exp_f32_e32 v154, v46
	v_exp_f32_e32 v155, v47
	ds_read_b64_tr_b16 v[62:63], v215 offset:0x2a00
	v_cvt_pk_bf16_f32 v147, v158, v159
	v_mfma_f32_32x32x16_bf16 v[112:127], a[208:211], a[144:147], v[112:127]
	ds_read_b64_tr_b16 v[56:57], v215 offset:0x2400
	v_cvt_pk_bf16_f32 v52, v48, v49
	v_add_f32_e32 v32, v236, v48
	v_add_f32_e32 v33, v235, v49
	s_add_i32 s12, s28, 0x80000
	s_mov_b32 s0, s12
	v_mfma_f32_32x32x16_bf16 v[96:111], a[208:211], a[176:179], v[96:111]
	ds_read_b64_tr_b16 v[58:59], v215 offset:0x2c00
	v_cvt_pk_bf16_f32 v53, v50, v51
	v_add_f32_e32 v32, v32, v50
	v_add_f32_e32 v33, v33, v51
	v_mfma_f32_32x32x16_bf16 v[80:95], a[240:243], a[144:147], v[80:95]
	ds_read_b64_tr_b16 v[48:49], v215 offset:0x2600
	v_cvt_pk_bf16_f32 v54, v218, v219
	v_add_f32_e32 v32, v32, v218
	v_add_f32_e32 v33, v33, v219
	s_add_i32 s1, s28, 0x80400
	v_mfma_f32_32x32x16_bf16 v[64:79], a[240:243], a[176:179], v[64:79]
	ds_read_b64_tr_b16 v[50:51], v215 offset:0x2e00
	ds_read_b64_tr_b16 v[44:45], v215 offset:0x3000
	v_cvt_pk_bf16_f32 v55, v230, v231
	v_add_f32_e32 v32, v32, v230
	v_add_f32_e32 v33, v33, v231
	v_mfma_f32_32x32x16_bf16 v[112:127], a[212:215], a[148:151], v[112:127]
	ds_read_b64_tr_b16 v[46:47], v215 offset:0x3800
	v_add_f32_e32 v32, v32, v220
	v_add_f32_e32 v33, v33, v221
	s_add_i32 s13, s28, 0x80800
	s_mov_b32 s14, s13
	v_mfma_f32_32x32x16_bf16 v[96:111], a[212:215], a[180:183], v[96:111]
	ds_read_b64_tr_b16 v[40:41], v215 offset:0x3200
	v_add_f32_e32 v32, v32, v222
	v_add_f32_e32 v33, v33, v223
	v_mfma_f32_32x32x16_bf16 v[80:95], a[244:247], a[148:151], v[80:95]
	ds_read_b64_tr_b16 v[42:43], v215 offset:0x3a00
	v_add_f32_e32 v32, v32, v224
	v_add_f32_e32 v33, v33, v227
	s_add_i32 s15, s28, 0x80c00
	v_mfma_f32_32x32x16_bf16 v[64:79], a[244:247], a[180:183], v[64:79]
	ds_read_b64_tr_b16 v[36:37], v215 offset:0x3400
	ds_read_b64_tr_b16 v[38:39], v215 offset:0x3c00
	v_add_f32_e32 v156, v32, v228
	v_add_f32_e32 v157, v33, v229
	v_mfma_f32_32x32x16_bf16 v[112:127], a[216:219], a[152:155], v[112:127]
	ds_read_b64_tr_b16 v[32:33], v215 offset:0x3600
	v_cvt_pk_bf16_f32 v140, v141, v142
	v_add_f32_e32 v158, v237, v141
	v_add_f32_e32 v142, v238, v142
	s_add_i32 s27, s63, 0x0
	v_mfma_f32_32x32x16_bf16 v[96:111], a[216:219], a[184:187], v[96:111]
	ds_read_b64_tr_b16 v[34:35], v215 offset:0x3e00
	v_cvt_pk_bf16_f32 v141, v143, v232
	v_add_f32_e32 v143, v158, v143
	v_add_f32_e32 v158, v142, v232
	v_mfma_f32_32x32x16_bf16 v[80:95], a[248:251], a[152:155], v[80:95]
	v_cvt_pk_bf16_f32 v142, v233, v234
	v_add_f32_e32 v159, v143, v233
	v_add_f32_e32 v158, v158, v234
	v_mfma_f32_32x32x16_bf16 v[64:79], a[248:251], a[184:187], v[64:79]
	s_add_i32 s30, s63, 0x80
	v_cvt_pk_bf16_f32 v143, v239, v240
	v_add_f32_e32 v159, v159, v239
	v_add_f32_e32 v158, v158, v240
	v_mfma_f32_32x32x16_bf16 v[112:127], a[220:223], a[156:159], v[112:127]
	v_add_f32_e32 v159, v159, v148
	v_add_f32_e32 v158, v158, v149
	v_mfma_f32_32x32x16_bf16 v[96:111], a[220:223], a[188:191], v[96:111]
	s_add_i32 s31, s63, 0x800
	v_add_f32_e32 v159, v159, v150
	v_add_f32_e32 v158, v158, v151
	v_mfma_f32_32x32x16_bf16 v[80:95], a[252:255], a[156:159], v[80:95]
	v_add_f32_e32 v159, v159, v152
	v_add_f32_e32 v158, v158, v153
	v_mfma_f32_32x32x16_bf16 v[64:79], a[252:255], a[188:191], v[64:79]
	s_add_i32 s33, s63, 0x880
	v_add_f32_e32 v159, v159, v154
	v_add_f32_e32 v158, v158, v155
	s_nop 0
	s_nop 4
	v_add_f32_e32 v156, v156, v157
	s_waitcnt vmcnt(0) lgkmcnt(0)
	s_barrier
	v_mfma_f32_32x32x16_bf16 a[0:15], v[180:183], v[164:167], a[0:15]
	v_mov_b32_e32 v157, v156
	v_mfma_f32_32x32x16_bf16 a[16:31], v[180:183], v[192:195], a[16:31]
	s_nop 1
	v_permlane32_swap_b32_e32 v156, v157
	v_add_f32_e32 v156, v156, v157
	ds_read_b128 a[192:195], v217 offset:0
	v_mfma_f32_32x32x16_bf16 a[32:47], v[188:191], v[164:167], a[32:47]
	v_add_f32_e32 v219, v225, v156
	v_add_f32_e32 v156, v159, v158
	v_mov_b32_e32 v157, v156
	ds_read_b128 a[196:199], v199 offset:0
	v_mfma_f32_32x32x16_bf16 a[48:63], v[188:191], v[192:195], a[48:63]
	v_permlane32_swap_b32_e32 v156, v157
	v_add_f32_e32 v156, v156, v157
	ds_read_b128 a[200:203], v198 offset:0
	v_mfma_f32_32x32x16_bf16 a[64:79], v[176:179], v[164:167], a[64:79]
	v_add_f32_e32 v218, v226, v156
	s_mov_b32 m0, s23
	s_nop 0
	buffer_load_dwordx4 v196, s[4:7], s27 offen lds
	ds_read_b128 a[204:207], v197 offset:0
	v_mfma_f32_32x32x16_bf16 a[80:95], v[176:179], v[192:195], a[80:95]
	s_mov_b32 m0, s24
	s_nop 0
	buffer_load_dwordx4 v196, s[4:7], s30 offen lds
	ds_read_b128 a[208:211], v217 offset:128
	v_mfma_f32_32x32x16_bf16 a[96:111], v[184:187], v[164:167], a[96:111]
	s_mov_b32 m0, s25
	s_nop 0
	buffer_load_dwordx4 v196, s[4:7], s31 offen lds
	ds_read_b128 a[212:215], v199 offset:128
	v_mfma_f32_32x32x16_bf16 a[112:127], v[184:187], v[192:195], a[112:127]
	s_mov_b32 m0, s26
	s_nop 0
	buffer_load_dwordx4 v196, s[4:7], s33 offen lds
	ds_read_b128 a[216:219], v198 offset:128
	v_mfma_f32_32x32x16_bf16 a[0:15], v[172:175], v[128:131], a[0:15]
	ds_read_b128 a[220:223], v197 offset:128
	v_max3_f32 v156, v112, v113, v80
	v_max3_f32 v157, v114, v115, v81
	v_max3_f32 v156, v156, v82, v83
	v_mfma_f32_32x32x16_bf16 a[16:31], v[172:175], v[144:147], a[16:31]
	ds_read_b128 a[224:227], v217 offset:8192
	v_max3_f32 v156, v156, v116, v117
	v_max3_f32 v157, v157, v118, v119
	v_max3_f32 v156, v156, v84, v85
	v_max3_f32 v157, v157, v86, v87
	v_mfma_f32_32x32x16_bf16 a[32:47], v[168:171], v[128:131], a[32:47]
	ds_read_b128 a[228:231], v199 offset:8192
	v_max3_f32 v156, v156, v120, v121
	v_max3_f32 v157, v157, v122, v123
	v_max3_f32 v156, v156, v88, v89
	v_max3_f32 v157, v157, v90, v91
	v_mfma_f32_32x32x16_bf16 a[48:63], v[168:171], v[144:147], a[48:63]
	ds_read_b128 a[232:235], v198 offset:8192
	v_max3_f32 v156, v156, v124, v125
	v_max3_f32 v157, v157, v126, v127
	v_max3_f32 v156, v156, v92, v93
	v_max3_f32 v157, v157, v94, v95
	v_mfma_f32_32x32x16_bf16 a[64:79], v[160:163], v[128:131], a[64:79]
	ds_read_b128 a[236:239], v197 offset:8192
	v_max3_f32 v158, v96, v97, v64
	v_max3_f32 v159, v98, v99, v65
	v_max3_f32 v158, v158, v66, v67
	v_mfma_f32_32x32x16_bf16 a[80:95], v[160:163], v[144:147], a[80:95]
	ds_read_b128 a[240:243], v217 offset:8320
	v_max3_f32 v158, v158, v100, v101
	v_max3_f32 v159, v159, v102, v103
	v_max3_f32 v158, v158, v68, v69
	v_max3_f32 v159, v159, v70, v71
	v_mfma_f32_32x32x16_bf16 a[96:111], v[136:139], v[128:131], a[96:111]
	ds_read_b128 a[244:247], v199 offset:8320
	v_max3_f32 v128, v158, v104, v105
	v_max3_f32 v129, v159, v106, v107
	v_max3_f32 v128, v128, v72, v73
	v_max3_f32 v129, v129, v74, v75
	v_mfma_f32_32x32x16_bf16 a[112:127], v[136:139], v[144:147], a[112:127]
	ds_read_b128 a[248:251], v198 offset:8320
	v_max3_f32 v128, v128, v108, v109
	v_max3_f32 v129, v129, v110, v111
	v_max3_f32 v128, v128, v76, v77
	v_max3_f32 v130, v129, v78, v79
	v_mfma_f32_32x32x16_bf16 a[0:15], v[132:135], v[52:55], a[0:15]
	ds_read_b128 a[252:255], v197 offset:8320
	v_max_f32_e32 v129, v156, v157
	v_mov_b32_e32 v131, v129
	s_nop 1
	v_permlane32_swap_b32_e32 v129, v131
	v_max_f32_e32 v129, v129, v131
	v_mfma_f32_32x32x16_bf16 a[16:31], v[132:135], v[140:143], a[16:31]
	v_max_f32_e32 v128, v128, v130
	v_mov_b32_e32 v130, v128
	s_nop 1
	v_permlane32_swap_b32_e32 v128, v130
	v_max_f32_e32 v128, v128, v130
	v_max_f32_e32 v130, v129, v129
	v_max_f32_e32 v131, v128, v128
	v_max_f32_e32 v130, v130, v131
	s_mov_b32 s0, 0x41000000
	v_mfma_f32_32x32x16_bf16 a[32:47], v[60:63], v[52:55], a[32:47]
	v_cmp_lt_f32_e32 vcc, s0, v130
	s_cmp_lg_u64 vcc, 0
	s_cselect_b64 s[0:1], -1, 0
	s_cbranch_vccnz .LBB0_43

.LBB0_38:
	s_waitcnt lgkmcnt(0)
	v_mfma_f32_32x32x16_bf16 v[112:127], a[192:195], a[128:131], v[0:15]
	ds_read_b64_tr_b16 v[172:173], v212 offset:0
	v_exp_f32_e32 v227, v80
	v_exp_f32_e32 v228, v81
	v_cvt_pk_bf16_f32 v164, v128, v129
	v_exp_f32_e32 v82, v82
	v_exp_f32_e32 v83, v83
	v_mfma_f32_32x32x16_bf16 v[96:111], a[192:195], a[160:163], v[16:31]
	ds_read_b64_tr_b16 v[174:175], v212 offset:0x800
	v_cvt_pk_bf16_f32 v165, v130, v131
	v_exp_f32_e32 v84, v84
	v_exp_f32_e32 v85, v85
	v_mfma_f32_32x32x16_bf16 v[48:63], a[224:227], a[128:131], v[0:15]
	ds_read_b64_tr_b16 v[180:181], v212 offset:0x200
	v_cvt_pk_bf16_f32 v166, v132, v133
	v_mfma_f32_32x32x16_bf16 v[32:47], a[224:227], a[160:163], v[16:31]
	ds_read_b64_tr_b16 v[182:183], v212 offset:0xa00
	v_exp_f32_e32 v86, v86
	v_exp_f32_e32 v87, v87
	ds_read_b64_tr_b16 v[184:185], v212 offset:0x400
	v_cvt_pk_bf16_f32 v167, v134, v135
	v_exp_f32_e32 v80, v88
	v_exp_f32_e32 v81, v89
	v_mfma_f32_32x32x16_bf16 v[112:127], a[196:199], a[132:135], v[112:127]
	ds_read_b64_tr_b16 v[186:187], v212 offset:0xc00
	v_cvt_pk_bf16_f32 v160, v136, v137
	v_exp_f32_e32 v90, v90
	v_exp_f32_e32 v91, v91
	v_mfma_f32_32x32x16_bf16 v[96:111], a[196:199], a[164:167], v[96:111]
	ds_read_b64_tr_b16 v[192:193], v212 offset:0x600
	v_cvt_pk_bf16_f32 v161, v138, v139
	v_exp_f32_e32 v217, v92
	v_exp_f32_e32 v220, v93
	v_mfma_f32_32x32x16_bf16 v[48:63], a[228:231], a[132:135], v[48:63]
	ds_read_b64_tr_b16 v[194:195], v212 offset:0xe00
	v_cvt_pk_bf16_f32 v162, v140, v141
	v_mfma_f32_32x32x16_bf16 v[32:47], a[228:231], a[164:167], v[32:47]
	ds_read_b64_tr_b16 v[188:189], v212 offset:0x1000
	v_exp_f32_e32 v221, v94
	v_exp_f32_e32 v222, v95
	ds_read_b64_tr_b16 v[190:191], v212 offset:0x1800
	v_cvt_pk_bf16_f32 v163, v142, v143
	v_exp_f32_e32 v130, v64
	v_exp_f32_e32 v131, v65
	v_mfma_f32_32x32x16_bf16 v[112:127], a[200:203], a[136:139], v[112:127]
	ds_read_b64_tr_b16 v[176:177], v212 offset:0x1200
	v_cvt_pk_bf16_f32 v196, v144, v145
	v_exp_f32_e32 v138, v66
	v_exp_f32_e32 v139, v67
	v_mfma_f32_32x32x16_bf16 v[96:111], a[200:203], a[168:171], v[96:111]
	ds_read_b64_tr_b16 v[178:179], v212 offset:0x1a00
	v_cvt_pk_bf16_f32 v197, v146, v147
	v_mfma_f32_32x32x16_bf16 v[48:63], a[232:235], a[136:139], v[48:63]
	ds_read_b64_tr_b16 v[168:169], v212 offset:0x1400
	v_exp_f32_e32 v229, v68
	v_exp_f32_e32 v230, v69
	v_cvt_pk_bf16_f32 v198, v148, v149
	v_mfma_f32_32x32x16_bf16 v[32:47], a[232:235], a[168:171], v[32:47]
	ds_read_b64_tr_b16 v[170:171], v212 offset:0x1c00
	ds_read_b64_tr_b16 v[144:145], v212 offset:0x1600
	v_exp_f32_e32 v231, v70
	v_exp_f32_e32 v232, v71
	v_cvt_pk_bf16_f32 v199, v150, v151
	v_exp_f32_e32 v64, v72
	v_exp_f32_e32 v65, v73
	v_mfma_f32_32x32x16_bf16 v[112:127], a[204:207], a[140:143], v[112:127]
	ds_read_b64_tr_b16 v[146:147], v212 offset:0x1e00
	v_cvt_pk_bf16_f32 v148, v152, v153
	v_exp_f32_e32 v70, v74
	v_exp_f32_e32 v71, v75
	v_mfma_f32_32x32x16_bf16 v[96:111], a[204:207], a[172:175], v[96:111]
	ds_read_b64_tr_b16 v[140:141], v212 offset:0x2000
	v_cvt_pk_bf16_f32 v149, v154, v155
	v_exp_f32_e32 v154, v76
	v_exp_f32_e32 v155, v77
	v_mfma_f32_32x32x16_bf16 v[48:63], a[236:239], a[140:143], v[48:63]
	ds_read_b64_tr_b16 v[142:143], v212 offset:0x2800
	v_cvt_pk_bf16_f32 v150, v156, v157
	v_mfma_f32_32x32x16_bf16 v[32:47], a[236:239], a[172:175], v[32:47]
	ds_read_b64_tr_b16 v[66:67], v212 offset:0x2200
	v_exp_f32_e32 v156, v78
	v_exp_f32_e32 v157, v79
	ds_read_b64_tr_b16 v[68:69], v212 offset:0x2a00
	v_cvt_pk_bf16_f32 v151, v158, v159
	v_mfma_f32_32x32x16_bf16 v[112:127], a[208:211], a[144:147], v[112:127]
	ds_read_b64_tr_b16 v[132:133], v212 offset:0x2400
	v_cvt_pk_bf16_f32 v72, v227, v228
	v_add_f32_e32 v74, v226, v227
	v_add_f32_e32 v75, v224, v228
	s_add_i32 s0, s28, 0x84000
	v_mfma_f32_32x32x16_bf16 v[96:111], a[208:211], a[176:179], v[96:111]
	ds_read_b64_tr_b16 v[134:135], v212 offset:0x2c00
	v_cvt_pk_bf16_f32 v73, v82, v83
	v_add_f32_e32 v78, v74, v82
	v_add_f32_e32 v75, v75, v83
	v_mfma_f32_32x32x16_bf16 v[48:63], a[240:243], a[144:147], v[48:63]
	ds_read_b64_tr_b16 v[76:77], v212 offset:0x2600
	v_cvt_pk_bf16_f32 v74, v84, v85
	v_add_f32_e32 v84, v78, v84
	v_add_f32_e32 v85, v75, v85
	s_add_i32 s1, s28, 0x84400
	v_mfma_f32_32x32x16_bf16 v[32:47], a[240:243], a[176:179], v[32:47]
	ds_read_b64_tr_b16 v[78:79], v212 offset:0x2e00
	ds_read_b64_tr_b16 v[82:83], v212 offset:0x3000
	v_cvt_pk_bf16_f32 v75, v86, v87
	v_add_f32_e32 v86, v84, v86
	v_add_f32_e32 v87, v85, v87
	v_mfma_f32_32x32x16_bf16 v[112:127], a[212:215], a[148:151], v[112:127]
	ds_read_b64_tr_b16 v[84:85], v212 offset:0x3800
	v_add_f32_e32 v88, v86, v80
	v_add_f32_e32 v89, v87, v81
	s_add_i32 s4, s28, 0x84800
	v_mfma_f32_32x32x16_bf16 v[96:111], a[212:215], a[180:183], v[96:111]
	ds_read_b64_tr_b16 v[86:87], v212 offset:0x3200
	v_add_f32_e32 v92, v88, v90
	v_add_f32_e32 v93, v89, v91
	v_mfma_f32_32x32x16_bf16 v[48:63], a[244:247], a[148:151], v[48:63]
	ds_read_b64_tr_b16 v[88:89], v212 offset:0x3a00
	v_add_f32_e32 v128, v92, v217
	v_add_f32_e32 v129, v93, v220
	s_add_i32 s5, s28, 0x84c00
	v_mfma_f32_32x32x16_bf16 v[32:47], a[244:247], a[180:183], v[32:47]
	ds_read_b64_tr_b16 v[92:93], v212 offset:0x3400
	ds_read_b64_tr_b16 v[94:95], v212 offset:0x3c00
	v_add_f32_e32 v152, v128, v221
	v_add_f32_e32 v153, v129, v222
	v_mfma_f32_32x32x16_bf16 v[112:127], a[216:219], a[152:155], v[112:127]
	ds_read_b64_tr_b16 v[128:129], v212 offset:0x3600
	v_cvt_pk_bf16_f32 v136, v130, v131
	v_add_f32_e32 v158, v223, v130
	v_add_f32_e32 v159, v225, v131
	v_mfma_f32_32x32x16_bf16 v[96:111], a[216:219], a[184:187], v[96:111]
	ds_read_b64_tr_b16 v[130:131], v212 offset:0x3e00
	v_cvt_pk_bf16_f32 v137, v138, v139
	v_add_f32_e32 v158, v158, v138
	v_add_f32_e32 v139, v159, v139
	v_mfma_f32_32x32x16_bf16 v[48:63], a[248:251], a[152:155], v[48:63]
	v_cvt_pk_bf16_f32 v138, v229, v230
	v_add_f32_e32 v158, v158, v229
	v_add_f32_e32 v159, v139, v230
	v_mfma_f32_32x32x16_bf16 v[32:47], a[248:251], a[184:187], v[32:47]
	s_add_i32 s6, s28, 0x80080
	v_cvt_pk_bf16_f32 v139, v231, v232
	v_add_f32_e32 v158, v158, v231
	v_add_f32_e32 v159, v159, v232
	v_mfma_f32_32x32x16_bf16 v[112:127], a[220:223], a[156:159], v[112:127]
	v_add_f32_e32 v158, v158, v64
	v_add_f32_e32 v159, v159, v65
	v_mfma_f32_32x32x16_bf16 v[96:111], a[220:223], a[188:191], v[96:111]
	v_add_f32_e32 v158, v158, v70
	v_add_f32_e32 v159, v159, v71
	v_mfma_f32_32x32x16_bf16 v[48:63], a[252:255], a[156:159], v[48:63]
	v_add_f32_e32 v158, v158, v154
	v_add_f32_e32 v159, v159, v155
	v_mfma_f32_32x32x16_bf16 v[32:47], a[252:255], a[188:191], v[32:47]
	s_add_i32 s7, s28, 0x80880
	v_add_f32_e32 v158, v158, v156
	v_add_f32_e32 v159, v159, v157
	s_nop 0
	s_nop 4
	v_add_f32_e32 v152, v152, v153
	s_waitcnt vmcnt(0) lgkmcnt(0)
	s_barrier
	v_mfma_f32_32x32x16_bf16 a[0:15], v[172:175], v[164:167], a[0:15]
	v_mov_b32_e32 v153, v152
	v_mfma_f32_32x32x16_bf16 a[16:31], v[172:175], v[196:199], a[16:31]
	s_nop 1
	v_permlane32_swap_b32_e32 v152, v153
	v_add_f32_e32 v152, v152, v153
	v_mfma_f32_32x32x16_bf16 a[32:47], v[180:183], v[164:167], a[32:47]
	v_add_f32_e32 v153, v219, v152
	v_add_f32_e32 v152, v158, v159
	v_mov_b32_e32 v158, v152
	v_mfma_f32_32x32x16_bf16 a[48:63], v[180:183], v[196:199], a[48:63]
	s_nop 1
	v_permlane32_swap_b32_e32 v152, v158
	v_add_f32_e32 v152, v152, v158
	v_mfma_f32_32x32x16_bf16 a[64:79], v[184:187], v[164:167], a[64:79]
	v_add_f32_e32 v152, v218, v152
	v_mfma_f32_32x32x16_bf16 a[80:95], v[184:187], v[196:199], a[80:95]
	v_mfma_f32_32x32x16_bf16 a[96:111], v[192:195], v[164:167], a[96:111]
	v_mfma_f32_32x32x16_bf16 a[112:127], v[192:195], v[196:199], a[112:127]
	v_mfma_f32_32x32x16_bf16 a[0:15], v[188:191], v[160:163], a[0:15]
	v_max3_f32 v158, v112, v113, v48
	v_max3_f32 v159, v114, v115, v49
	v_max3_f32 v158, v158, v50, v51
	v_mfma_f32_32x32x16_bf16 a[16:31], v[188:191], v[148:151], a[16:31]
	v_max3_f32 v158, v158, v116, v117
	v_max3_f32 v159, v159, v118, v119
	v_max3_f32 v158, v158, v52, v53
	v_max3_f32 v159, v159, v54, v55
	v_mfma_f32_32x32x16_bf16 a[32:47], v[176:179], v[160:163], a[32:47]
	v_max3_f32 v158, v158, v120, v121
	v_max3_f32 v159, v159, v122, v123
	v_max3_f32 v158, v158, v56, v57
	v_max3_f32 v159, v159, v58, v59
	v_mfma_f32_32x32x16_bf16 a[48:63], v[176:179], v[148:151], a[48:63]
	v_max3_f32 v158, v158, v124, v125
	v_max3_f32 v159, v159, v126, v127
	v_max3_f32 v158, v158, v60, v61
	v_max3_f32 v159, v159, v62, v63
	v_mfma_f32_32x32x16_bf16 a[64:79], v[168:171], v[160:163], a[64:79]
	v_max3_f32 v164, v96, v97, v32
	v_max3_f32 v165, v98, v99, v33
	v_max3_f32 v164, v164, v34, v35
	v_mfma_f32_32x32x16_bf16 a[80:95], v[168:171], v[148:151], a[80:95]
	v_max3_f32 v164, v164, v100, v101
	v_max3_f32 v165, v165, v102, v103
	v_max3_f32 v164, v164, v36, v37
	v_max3_f32 v165, v165, v38, v39
	v_mfma_f32_32x32x16_bf16 a[96:111], v[144:147], v[160:163], a[96:111]
	v_max3_f32 v160, v164, v104, v105
	v_max3_f32 v161, v165, v106, v107
	v_max3_f32 v160, v160, v40, v41
	v_max3_f32 v161, v161, v42, v43
	v_mfma_f32_32x32x16_bf16 a[112:127], v[144:147], v[148:151], a[112:127]
	v_max3_f32 v145, v161, v110, v111
	v_max3_f32 v144, v160, v108, v109
	v_max3_f32 v146, v144, v44, v45
	v_max3_f32 v145, v145, v46, v47
	v_mfma_f32_32x32x16_bf16 a[0:15], v[140:143], v[72:75], a[0:15]
	v_max_f32_e32 v144, v158, v159
	v_mov_b32_e32 v147, v144
	s_nop 1
	v_permlane32_swap_b32_e32 v144, v147
	v_max_f32_e32 v144, v144, v147
	v_mfma_f32_32x32x16_bf16 a[16:31], v[140:143], v[136:139], a[16:31]
	v_max_f32_e32 v140, v146, v145
	v_mov_b32_e32 v141, v140
	s_nop 1
	v_permlane32_swap_b32_e32 v140, v141
	v_max_f32_e32 v140, v140, v141
	v_max_f32_e32 v141, v144, v144
	v_max_f32_e32 v142, v140, v140
	v_max_f32_e32 v141, v141, v142
	s_mov_b32 s0, 0x41000000
	v_mfma_f32_32x32x16_bf16 a[32:47], v[66:69], v[72:75], a[32:47]
	v_cmp_lt_f32_e32 vcc, s0, v141
	s_cmp_lg_u64 vcc, 0
	s_cselect_b64 s[0:1], -1, 0
	s_cbranch_vccnz .LBB0_45
